# RMSNorm / router row loops: read-once residual-row loads carry the nt hint (on top of the final-phase nt version)
# baseline (speedup 1.0000x reference)
; __device__ __forceinline__ unsigned pk2(float lo, float hi) { return f2bf(lo) | (f2bf(hi) << 16); }
; __device__ __forceinline__ float rms_row_load(const float* xrow, int lane, f32x4 (&v)[8]) {
;     const f32x4* xr = (const f32x4*)xrow + lane; float s = 0.f;
; #pragma unroll
;     for (int j = 0; j < 8; ++j) { v[j] = xr[64 * j]; s += (v[j].x * v[j].x + v[j].y * v[j].y) + (v[j].z * v[j].z + v[j].w * v[j].w); }
;     return 1.0f / sqrtf(wave_sum(s) * (1.0f / D) + EPS);
; }
; __device__ __forceinline__ void rms_row_to_bf16(const float* xrow, const float* gain, bf16* orow, int lane) {
;     f32x4 v[8]; const float rstd = rms_row_load(xrow, lane, v);
;     const f32x4* gr = (const f32x4*)gain + lane; unsigned long long* o8 = (unsigned long long*)orow + lane;
; #pragma unroll
;     for (int j = 0; j < 8; ++j) { const f32x4 g = gr[64 * j]; o8[64 * j] = (unsigned long long)pk2(v[j].x * rstd * g.x, v[j].y * rstd * g.y) | ((unsigned long long)pk2(v[j].z * rstd * g.z, v[j].w * rstd * g.w) << 32); }
.LBB0_67:
	global_load_dwordx4 v[14:17], v[30:31], off offset:-3072 nt
	global_load_dwordx4 v[10:13], v[30:31], off offset:-2048 nt
	global_load_dwordx4 v[6:9], v[30:31], off offset:-1024 nt
	global_load_dwordx4 v[2:5], v[30:31], off nt
	v_add_co_u32_e32 v60, vcc, 0xfffff000, v30
	global_load_dwordx4 v[40:43], v[18:19], off nt
	s_nop 0
	v_addc_co_u32_e32 v61, vcc, -1, v31, vcc
	global_load_dwordx4 v[44:47], v[60:61], off offset:-3072 nt
	global_load_dwordx4 v[48:51], v[60:61], off offset:-2048 nt
	global_load_dwordx4 v[52:55], v[60:61], off offset:-1024 nt
	global_load_dwordx4 v[56:59], v[30:31], off offset:-4096 nt
	s_add_i32 s12, s12, s76
	s_cmpk_lt_i32 s12, 0x2000
	v_lshl_add_u64 v[30:31], v[30:31], 0, s[14:15]
	s_waitcnt vmcnt(8)
	v_mul_f32_e32 v39, v15, v15
	v_mul_f32_e32 v60, v17, v17
	s_waitcnt vmcnt(7)
	v_mul_f32_e32 v61, v11, v11
	v_mul_f32_e32 v62, v13, v13
	s_waitcnt vmcnt(6)
	v_mul_f32_e32 v63, v7, v7
	v_mul_f32_e32 v64, v9, v9
	s_waitcnt vmcnt(5)
	v_mul_f32_e32 v65, v3, v3
	v_mul_f32_e32 v66, v5, v5
	v_fmac_f32_e32 v39, v14, v14
	v_fmac_f32_e32 v60, v16, v16
	v_fmac_f32_e32 v61, v10, v10
	v_fmac_f32_e32 v62, v12, v12
	v_fmac_f32_e32 v63, v6, v6
	v_fmac_f32_e32 v64, v8, v8
	v_fmac_f32_e32 v65, v2, v2
	v_fmac_f32_e32 v66, v4, v4
	s_waitcnt vmcnt(3)
	v_mul_f32_e32 v67, v45, v45
	v_mul_f32_e32 v68, v47, v47
	v_add_f32_e32 v39, v39, v60
	s_waitcnt vmcnt(2)
	v_mul_f32_e32 v60, v49, v49
	v_add_f32_e32 v61, v61, v62
	v_mul_f32_e32 v62, v51, v51
	v_add_f32_e32 v63, v63, v64
	v_add_f32_e32 v64, v65, v66
	s_waitcnt vmcnt(1)
	v_mul_f32_e32 v65, v53, v53
	v_mul_f32_e32 v66, v55, v55
	v_fmac_f32_e32 v67, v44, v44
	v_fmac_f32_e32 v68, v46, v46
	v_fmac_f32_e32 v60, v48, v48
	v_fmac_f32_e32 v62, v50, v50
	s_waitcnt vmcnt(0)
	v_mul_f32_e32 v69, v57, v57
	v_mul_f32_e32 v70, v59, v59
	v_fmac_f32_e32 v65, v52, v52
	v_fmac_f32_e32 v66, v54, v54
	v_add_f32_e32 v67, v67, v68
	v_add_f32_e32 v60, v60, v62
	v_fmac_f32_e32 v69, v56, v56
	v_fmac_f32_e32 v70, v58, v58
	v_add_f32_e32 v62, v65, v66
	v_add_f32_e32 v60, v67, v60
	v_add_f32_e32 v65, v69, v70
	v_add_f32_e32 v60, v60, v62
	v_add_f32_e32 v60, v60, v65
	v_add_f32_e32 v39, v60, v39
	v_add_f32_e32 v39, v39, v61
	v_add_f32_e32 v39, v39, v63
	v_add_f32_e32 v39, v39, v64
	ds_bpermute_b32 v60, v32, v39
	s_waitcnt lgkmcnt(0)
	v_add_f32_e32 v39, v39, v60
	ds_bpermute_b32 v60, v33, v39
	s_waitcnt lgkmcnt(0)
	v_add_f32_e32 v39, v39, v60
	ds_bpermute_b32 v60, v34, v39
	s_waitcnt lgkmcnt(0)
	v_add_f32_e32 v39, v39, v60
	ds_bpermute_b32 v60, v35, v39
	s_waitcnt lgkmcnt(0)
	v_add_f32_e32 v39, v39, v60
	ds_bpermute_b32 v60, v36, v39
	s_waitcnt lgkmcnt(0)
	v_add_f32_e32 v39, v39, v60
	ds_bpermute_b32 v60, v37, v39
	s_waitcnt lgkmcnt(0)
; __device__ __forceinline__ unsigned pk2(float lo, float hi) { return f2bf(lo) | (f2bf(hi) << 16); }
; __device__ __forceinline__ float rms_row_load(const float* xrow, int lane, f32x4 (&v)[8]) {
;     ...
;     return 1.0f / sqrtf(wave_sum(s) * (1.0f / D) + EPS);
; }
; __device__ __forceinline__ void rms_row_to_bf16(const float* xrow, const float* gain, bf16* orow, int lane) {
;     f32x4 v[8]; const float rstd = rms_row_load(xrow, lane, v);
;     const f32x4* gr = (const f32x4*)gain + lane; unsigned long long* o8 = (unsigned long long*)orow + lane;
; #pragma unroll
;     for (int j = 0; j < 8; ++j) { const f32x4 g = gr[64 * j]; o8[64 * j] = (unsigned long long)pk2(v[j].x * rstd * g.x, v[j].y * rstd * g.y) | ((unsigned long long)pk2(v[j].z * rstd * g.z, v[j].w * rstd * g.w) << 32); }
	v_add_f32_e32 v39, v39, v60
	v_fmamk_f32 v39, v39, 0x3a000000, v1
	v_mul_f32_e32 v60, 0x4f800000, v39
	v_cmp_gt_f32_e32 vcc, s3, v39
	s_nop 1
	v_cndmask_b32_e32 v39, v39, v60, vcc
	v_sqrt_f32_e32 v60, v39
	s_nop 0
	v_add_u32_e32 v61, -1, v60
	v_add_u32_e32 v62, 1, v60
	v_fma_f32 v63, -v61, v60, v39
	v_fma_f32 v64, -v62, v60, v39
	v_cmp_ge_f32_e64 s[4:5], 0, v63
	s_nop 1
	v_cndmask_b32_e64 v60, v60, v61, s[4:5]
	v_cmp_lt_f32_e64 s[4:5], 0, v64
	s_nop 1
	v_cndmask_b32_e64 v60, v60, v62, s[4:5]
	v_mul_f32_e32 v61, 0x37800000, v60
	v_cndmask_b32_e32 v60, v60, v61, vcc
	v_cmp_class_f32_e32 vcc, v39, v38
	s_nop 1
	v_cndmask_b32_e32 v39, v60, v39, vcc
	v_div_scale_f32 v60, s[4:5], v39, v39, 1.0
	v_rcp_f32_e32 v62, v60
	v_div_scale_f32 v61, vcc, 1.0, v39, 1.0
	v_fma_f32 v63, -v60, v62, 1.0
	v_fmac_f32_e32 v62, v63, v62
	v_mul_f32_e32 v63, v61, v62
	v_fma_f32 v64, -v60, v63, v61
	v_fmac_f32_e32 v63, v64, v62
	v_fma_f32 v60, -v60, v63, v61
	v_div_fmas_f32 v60, v60, v62, v63
	v_div_fixup_f32 v39, v60, v39, 1.0
	v_mul_f32_e32 v44, v44, v39
	v_mul_f32_e32 v46, v46, v39
	v_mul_f32_e32 v45, v45, v39
	v_mul_f32_e32 v47, v47, v39
	v_mul_f32_e32 v40, v40, v44
	v_mul_f32_e32 v42, v42, v46
	v_mul_f32_e32 v41, v41, v45
	v_mul_f32_e32 v43, v43, v47
	v_bfe_u32 v44, v40, 16, 1
	v_bfe_u32 v46, v42, 16, 1
	v_bfe_u32 v45, v41, 16, 1
	v_bfe_u32 v47, v43, 16, 1
	v_add3_u32 v40, v40, v44, s13
	v_add3_u32 v42, v42, v46, s13
	v_add3_u32 v41, v41, v45, s13
	v_add3_u32 v43, v43, v47, s13
	v_lshrrev_b32_e32 v40, 16, v40
	v_lshrrev_b32_e32 v42, 16, v42
	v_and_or_b32 v40, v41, s16, v40
	v_and_or_b32 v41, v43, s16, v42
	global_store_dwordx2 v[28:29], v[40:41], off offset:-3584
	v_mul_f32_e32 v48, v48, v39
	v_mul_f32_e32 v50, v50, v39
	v_mul_f32_e32 v49, v49, v39
	v_mul_f32_e32 v44, v51, v39
	v_mul_f32_e32 v14, v14, v39
	v_mul_f32_e32 v16, v16, v39
	v_mul_f32_e32 v15, v15, v39
	v_mul_f32_e32 v17, v17, v39
	v_mul_f32_e32 v10, v10, v39
	v_mul_f32_e32 v12, v12, v39
	v_mul_f32_e32 v11, v11, v39
	v_mul_f32_e32 v13, v13, v39
	v_mul_f32_e32 v6, v6, v39
	v_mul_f32_e32 v8, v8, v39
	v_mul_f32_e32 v7, v7, v39
	v_mul_f32_e32 v9, v9, v39
	v_mul_f32_e32 v2, v2, v39
	v_mul_f32_e32 v4, v4, v39
	v_mul_f32_e32 v3, v3, v39
	v_mul_f32_e32 v5, v5, v39
	v_mul_f32_e32 v40, v100, v48
	v_mul_f32_e32 v42, v102, v50
	v_mul_f32_e32 v41, v101, v49
	v_mul_f32_e32 v43, v103, v44
	v_bfe_u32 v44, v40, 16, 1
	v_bfe_u32 v46, v42, 16, 1
	v_bfe_u32 v45, v41, 16, 1
	v_bfe_u32 v47, v43, 16, 1
	v_add3_u32 v40, v40, v44, s13
	v_add3_u32 v42, v42, v46, s13
	v_add3_u32 v41, v41, v45, s13
	v_add3_u32 v43, v43, v47, s13
	v_lshrrev_b32_e32 v40, 16, v40
	v_lshrrev_b32_e32 v42, 16, v42
	v_and_or_b32 v40, v41, s16, v40
	v_and_or_b32 v41, v43, s16, v42
	global_store_dwordx2 v[28:29], v[40:41], off offset:-3072
	v_mul_f32_e32 v44, v52, v39
	v_mul_f32_e32 v46, v54, v39
	v_mul_f32_e32 v45, v53, v39
	v_mul_f32_e32 v47, v55, v39
	v_mul_f32_e32 v40, v104, v44
	v_mul_f32_e32 v42, v106, v46
	v_mul_f32_e32 v41, v105, v45
	v_mul_f32_e32 v43, v107, v47
	v_bfe_u32 v44, v40, 16, 1
	v_bfe_u32 v46, v42, 16, 1
	v_bfe_u32 v45, v41, 16, 1
	v_bfe_u32 v47, v43, 16, 1
	v_add3_u32 v40, v40, v44, s13
	v_add3_u32 v42, v42, v46, s13
	v_add3_u32 v41, v41, v45, s13
	v_add3_u32 v43, v43, v47, s13
	v_lshrrev_b32_e32 v40, 16, v40
	v_lshrrev_b32_e32 v42, 16, v42
	v_and_or_b32 v40, v41, s16, v40
	v_and_or_b32 v41, v43, s16, v42
	global_store_dwordx2 v[28:29], v[40:41], off offset:-2560
	v_mul_f32_e32 v44, v56, v39
	v_mul_f32_e32 v46, v58, v39
	v_mul_f32_e32 v45, v57, v39
	v_mul_f32_e32 v47, v59, v39
	v_mul_f32_e32 v40, v44, v108
	v_mul_f32_e32 v42, v46, v110
	v_mul_f32_e32 v41, v45, v109
	v_mul_f32_e32 v43, v47, v111
	v_bfe_u32 v44, v40, 16, 1
	v_bfe_u32 v46, v42, 16, 1
	v_bfe_u32 v45, v41, 16, 1
	v_bfe_u32 v47, v43, 16, 1
	v_add3_u32 v40, v40, v44, s13
	v_add3_u32 v42, v42, v46, s13
	v_add3_u32 v41, v41, v45, s13
	v_add3_u32 v43, v43, v47, s13
	v_lshrrev_b32_e32 v40, 16, v40
	v_lshrrev_b32_e32 v42, 16, v42
	v_and_or_b32 v40, v41, s16, v40
	v_and_or_b32 v41, v43, s16, v42
	global_store_dwordx2 v[28:29], v[40:41], off offset:-2048
	v_mul_f32_e32 v14, v14, v112
	v_mul_f32_e32 v16, v16, v114
	v_mul_f32_e32 v15, v15, v113
	v_mul_f32_e32 v17, v17, v115
	v_bfe_u32 v40, v14, 16, 1
	v_bfe_u32 v42, v16, 16, 1
	v_bfe_u32 v41, v15, 16, 1
	v_bfe_u32 v43, v17, 16, 1
	v_add3_u32 v14, v14, v40, s13
	v_add3_u32 v16, v16, v42, s13
	v_add3_u32 v15, v15, v41, s13
	v_add3_u32 v17, v17, v43, s13
	v_lshrrev_b32_e32 v14, 16, v14
	v_lshrrev_b32_e32 v16, 16, v16
	v_and_or_b32 v14, v15, s16, v14
	v_and_or_b32 v15, v17, s16, v16
	global_store_dwordx2 v[28:29], v[14:15], off offset:-1536
	v_mul_f32_e32 v10, v10, v116
	v_mul_f32_e32 v12, v12, v118
	v_mul_f32_e32 v11, v11, v117
	v_mul_f32_e32 v13, v13, v119
	v_bfe_u32 v14, v10, 16, 1
	v_bfe_u32 v16, v12, 16, 1
	v_bfe_u32 v15, v11, 16, 1
	v_bfe_u32 v17, v13, 16, 1
	v_add3_u32 v10, v10, v14, s13
	v_add3_u32 v12, v12, v16, s13
	v_add3_u32 v11, v11, v15, s13
	v_add3_u32 v13, v13, v17, s13
	v_lshrrev_b32_e32 v10, 16, v10
	v_lshrrev_b32_e32 v12, 16, v12
	v_and_or_b32 v10, v11, s16, v10
	v_and_or_b32 v11, v13, s16, v12
	global_store_dwordx2 v[28:29], v[10:11], off offset:-1024
	v_mul_f32_e32 v6, v6, v120
	v_mul_f32_e32 v8, v8, v122
	v_mul_f32_e32 v7, v7, v121
	v_mul_f32_e32 v9, v9, v123
	v_bfe_u32 v10, v6, 16, 1
	v_bfe_u32 v12, v8, 16, 1
	v_bfe_u32 v11, v7, 16, 1
	v_bfe_u32 v13, v9, 16, 1
	v_add3_u32 v6, v6, v10, s13
	v_add3_u32 v8, v8, v12, s13
	v_add3_u32 v7, v7, v11, s13
	v_add3_u32 v9, v9, v13, s13
	v_lshrrev_b32_e32 v6, 16, v6
	v_lshrrev_b32_e32 v8, 16, v8
	v_and_or_b32 v6, v7, s16, v6
	v_and_or_b32 v7, v9, s16, v8
	global_store_dwordx2 v[28:29], v[6:7], off offset:-512
	v_mul_f32_e32 v2, v2, v124
	v_mul_f32_e32 v4, v4, v126
	v_mul_f32_e32 v3, v3, v125
	v_mul_f32_e32 v5, v5, v127
	v_bfe_u32 v6, v2, 16, 1
	v_bfe_u32 v8, v4, 16, 1
	v_bfe_u32 v7, v3, 16, 1
	v_bfe_u32 v9, v5, 16, 1
	v_add3_u32 v2, v2, v6, s13
	v_add3_u32 v4, v4, v8, s13
	v_add3_u32 v3, v3, v7, s13
	v_add3_u32 v5, v5, v9, s13
	v_lshrrev_b32_e32 v2, 16, v2
	v_lshrrev_b32_e32 v4, 16, v4
	v_and_or_b32 v2, v3, s16, v2
	v_and_or_b32 v3, v5, s16, v4
	global_store_dwordx2 v[28:29], v[2:3], off
	v_lshl_add_u64 v[28:29], v[28:29], 0, s[6:7]
	s_cbranch_scc1 .LBB0_67

; #define LAS __attribute__((address_space(3)))
; __device__ __forceinline__ unsigned pk2(float lo, float hi) { return f2bf(lo) | (f2bf(hi) << 16); }
; __device__ __forceinline__ float rms_row_load(const float* xrow, int lane, f32x4 (&v)[8]) {
;     const f32x4* xr = (const f32x4*)xrow + lane; float s = 0.f;
; #pragma unroll
;     for (int j = 0; j < 8; ++j) { v[j] = xr[64 * j]; s += (v[j].x * v[j].x + v[j].y * v[j].y) + (v[j].z * v[j].z + v[j].w * v[j].w); }
;     return 1.0f / sqrtf(wave_sum(s) * (1.0f / D) + EPS);
; __global__ void __launch_bounds__(NWAVES * 64, 2) trunk_fwd(Args args) {
;     ...
;                 for (int m = r0 + wave; m < r1; m += NWAVES) {
;                     f32x4 v[8]; const float rstd = rms_row_load(XA + (size_t)m * D, lane, v);
;                     const f32x4* gr = (const f32x4*)gain + lane; unsigned long long* o8 = (unsigned long long*)(Hb + (size_t)m * D) + lane;
;                     float lg[8];
; #pragma unroll
;                     for (int e = 0; e < 8; ++e) lg[e] = 0.f;
; #pragma unroll
;                     for (int jj = 0; jj < 8; ++jj) { const f32x4 gg = gr[64 * jj]; const float a0 = v[jj].x * rstd * gg.x, a1 = v[jj].y * rstd * gg.y, a2 = v[jj].z * rstd * gg.z, a3 = v[jj].w * rstd * gg.w;
;                         o8[64 * jj] = (unsigned long long)pk2(a0, a1) | ((unsigned long long)pk2(a2, a3) << 32);
;                         const int c0 = 256 * jj + 4 * lane; const float av[4] = {a0, a1, a2, a3};
; #pragma unroll
;                         for (int q = 0; q < 4; ++q) { const f32x4 w0 = *(const LAS f32x4*)(RW + (c0 + q) * 8), w1 = *(const LAS f32x4*)(RW + (c0 + q) * 8 + 4);
;                             lg[0] += av[q] * w0.x; lg[1] += av[q] * w0.y; lg[2] += av[q] * w0.z; lg[3] += av[q] * w0.w; lg[4] += av[q] * w1.x; lg[5] += av[q] * w1.y; lg[6] += av[q] * w1.z; lg[7] += av[q] * w1.w; } }
.LBB0_770:
	v_readlane_b32 s4, v250, 6
	v_readlane_b32 s5, v250, 7
	s_mov_b32 s0, 0x36da2000
	s_nop 0
	v_lshl_add_u64 v[2:3], s[4:5], 0, v[56:57]
	v_add_co_u32_e32 v4, vcc, 0x36da1000, v2
	s_nop 1
	v_addc_co_u32_e32 v5, vcc, 0, v3, vcc
	global_load_dwordx4 v[30:33], v[4:5], off nt
	global_load_dwordx4 v[26:29], v[4:5], off offset:1024 nt
	global_load_dwordx4 v[22:25], v[4:5], off offset:2048 nt
	global_load_dwordx4 v[18:21], v[4:5], off offset:3072 nt
	v_add_co_u32_e32 v2, vcc, s0, v2
	s_mov_b32 s0, 0xf800000
	s_nop 0
	v_addc_co_u32_e32 v3, vcc, 0, v3, vcc
	s_waitcnt lgkmcnt(0)
	global_load_dwordx4 v[14:17], v[2:3], off nt
	global_load_dwordx4 v[10:13], v[2:3], off offset:1024 nt
	global_load_dwordx4 v[6:9], v[2:3], off offset:2048 nt
	global_load_dwordx4 v[2:5], v[2:3], off offset:3072 nt
	s_waitcnt vmcnt(7)
	v_mul_f32_e32 v34, v31, v31
	v_mul_f32_e32 v133, v33, v33
	v_fmac_f32_e32 v34, v30, v30
	v_fmac_f32_e32 v133, v32, v32
	v_add_f32_e32 v34, v34, v133
	s_waitcnt vmcnt(6)
	v_mul_f32_e32 v132, v27, v27
	v_mul_f32_e32 v133, v29, v29
	v_fmac_f32_e32 v132, v26, v26
	v_fmac_f32_e32 v133, v28, v28
	v_add_f32_e32 v132, v132, v133
	v_add_f32_e32 v34, v34, v132
	s_waitcnt vmcnt(5)
	v_mul_f32_e32 v132, v23, v23
	v_mul_f32_e32 v133, v25, v25
	v_fmac_f32_e32 v132, v22, v22
	v_fmac_f32_e32 v133, v24, v24
	v_add_f32_e32 v132, v132, v133
	v_add_f32_e32 v34, v34, v132
	s_waitcnt vmcnt(4)
	v_mul_f32_e32 v132, v19, v19
	v_mul_f32_e32 v133, v21, v21
	v_fmac_f32_e32 v132, v18, v18
	v_fmac_f32_e32 v133, v20, v20
	v_add_f32_e32 v132, v132, v133
	v_add_f32_e32 v34, v34, v132
	s_waitcnt vmcnt(3)
	v_mul_f32_e32 v132, v15, v15
	v_mul_f32_e32 v133, v17, v17
	v_fmac_f32_e32 v132, v14, v14
	v_fmac_f32_e32 v133, v16, v16
	v_add_f32_e32 v132, v132, v133
	v_add_f32_e32 v34, v34, v132
	s_waitcnt vmcnt(2)
	v_mul_f32_e32 v132, v11, v11
	v_mul_f32_e32 v133, v13, v13
	v_fmac_f32_e32 v132, v10, v10
	v_fmac_f32_e32 v133, v12, v12
	v_add_f32_e32 v132, v132, v133
	v_add_f32_e32 v34, v34, v132
	s_waitcnt vmcnt(1)
	v_mul_f32_e32 v132, v7, v7
	v_mul_f32_e32 v133, v9, v9
	v_fmac_f32_e32 v132, v6, v6
	v_fmac_f32_e32 v133, v8, v8
	v_add_f32_e32 v132, v132, v133
	v_add_f32_e32 v34, v34, v132
	s_waitcnt vmcnt(0)
	v_mul_f32_e32 v132, v3, v3
	v_mul_f32_e32 v133, v5, v5
	v_fmac_f32_e32 v132, v2, v2
	v_fmac_f32_e32 v133, v4, v4
	v_add_f32_e32 v132, v132, v133
	v_add_f32_e32 v34, v34, v132
	ds_bpermute_b32 v35, v43, v34
	s_waitcnt lgkmcnt(0)
	v_add_f32_e32 v34, v34, v35
	ds_bpermute_b32 v35, v63, v34
	s_waitcnt lgkmcnt(0)
	v_add_f32_e32 v34, v34, v35
	ds_bpermute_b32 v35, v65, v34
	s_waitcnt lgkmcnt(0)
	v_add_f32_e32 v34, v34, v35
	ds_bpermute_b32 v35, v67, v34
	s_waitcnt lgkmcnt(0)
	v_add_f32_e32 v34, v34, v35
	ds_bpermute_b32 v35, v69, v34
	s_waitcnt lgkmcnt(0)
	v_add_f32_e32 v34, v34, v35
	ds_bpermute_b32 v35, v71, v34
	s_waitcnt lgkmcnt(0)
	v_add_f32_e32 v34, v34, v35
	v_fmamk_f32 v34, v34, 0x3a000000, v226
	v_cmp_gt_f32_e32 vcc, s0, v34
	v_mul_f32_e32 v35, 0x4f800000, v34
	s_nop 0
	v_cndmask_b32_e32 v34, v34, v35, vcc
	v_sqrt_f32_e32 v35, v34
	s_nop 0
	v_add_u32_e32 v36, -1, v35
	v_fma_f32 v37, -v36, v35, v34
	v_cmp_ge_f32_e64 s[0:1], 0, v37
	v_add_u32_e32 v37, 1, v35
	s_nop 0
	v_cndmask_b32_e64 v36, v35, v36, s[0:1]
	v_fma_f32 v35, -v37, v35, v34
	v_cmp_lt_f32_e64 s[0:1], 0, v35
	s_nop 1
	v_cndmask_b32_e64 v35, v36, v37, s[0:1]
	v_mul_f32_e32 v36, 0x37800000, v35
	v_cndmask_b32_e32 v35, v35, v36, vcc
	v_cmp_class_f32_e32 vcc, v34, v225
	s_nop 1
	v_cndmask_b32_e32 v34, v35, v34, vcc
	v_div_scale_f32 v35, s[0:1], v34, v34, 1.0
	v_rcp_f32_e32 v36, v35
	s_mov_b32 s0, 0x34da1000
	v_fma_f32 v37, -v35, v36, 1.0
	v_fmac_f32_e32 v36, v37, v36
	v_div_scale_f32 v37, vcc, 1.0, v34, 1.0
	v_mul_f32_e32 v38, v37, v36
	v_fma_f32 v39, -v35, v38, v37
	v_fmac_f32_e32 v38, v39, v36
	v_fma_f32 v35, -v35, v38, v37
	v_div_fmas_f32 v35, v35, v36, v38
	v_div_fixup_f32 v80, v35, v34, 1.0
	v_mul_f32_e32 v30, v80, v30
	v_lshl_add_u64 v[34:35], s[4:5], 0, v[54:55]
	v_add_co_u32_e32 v58, vcc, s0, v34
	v_mul_f32_e32 v26, v80, v26
	s_nop 0
	v_addc_co_u32_e32 v59, vcc, 0, v35, vcc
	v_mul_f32_e32 v22, v80, v22
	v_mul_f32_e32 v18, v80, v18
	v_mul_f32_e32 v14, v80, v14
	v_mul_f32_e32 v10, v80, v10
	v_mul_f32_e32 v6, v80, v6
	v_mul_f32_e32 v2, v80, v2
	v_mul_f32_e32 v60, v30, v100
	v_mul_f32_e32 v30, v80, v31
	v_mul_f32_e32 v62, v30, v101
	v_mul_f32_e32 v30, v80, v32
	v_mul_f32_e32 v64, v30, v102
	v_mul_f32_e32 v30, v80, v33
	v_mul_f32_e32 v66, v30, v103
	v_bfe_u32 v30, v60, 16, 1
	v_add3_u32 v30, v60, v30, s36
	v_bfe_u32 v31, v62, 16, 1
	v_lshrrev_b32_e32 v30, 16, v30
	v_add3_u32 v31, v62, v31, s36
	v_and_or_b32 v30, v31, s27, v30
	v_bfe_u32 v31, v64, 16, 1
	v_add3_u32 v31, v64, v31, s36
	v_bfe_u32 v32, v66, 16, 1
	v_lshrrev_b32_e32 v31, 16, v31
	v_add3_u32 v32, v66, v32, s36
	v_and_or_b32 v31, v32, s27, v31
	global_store_dwordx2 v[58:59], v[30:31], off
	ds_read_b128 v[30:33], v73
	ds_read_b128 v[38:41], v73 offset:16
	ds_read_b128 v[34:37], v73 offset:32
	ds_read_b128 v[82:85], v73 offset:48
	s_waitcnt lgkmcnt(3)
	v_fma_f32 v79, v60, v32, 0
	v_fma_f32 v78, v60, v33, 0
	s_waitcnt lgkmcnt(2)
	v_fma_f32 v77, v60, v38, 0
	v_fma_f32 v76, v60, v39, 0
	v_fma_f32 v75, v60, v40, 0
	v_fma_f32 v74, v60, v41, 0
	s_waitcnt lgkmcnt(1)
	v_fmac_f32_e32 v79, v62, v36
	v_fmac_f32_e32 v78, v62, v37
	s_waitcnt lgkmcnt(0)
	v_fmac_f32_e32 v77, v62, v82
	v_fmac_f32_e32 v76, v62, v83
	v_fmac_f32_e32 v75, v62, v84
	v_fmac_f32_e32 v74, v62, v85
	ds_read_b128 v[36:39], v73 offset:64
	ds_read_b128 v[82:85], v73 offset:80
	s_waitcnt lgkmcnt(1)
	v_fmac_f32_e32 v79, v64, v38
	v_fmac_f32_e32 v78, v64, v39
	s_waitcnt lgkmcnt(0)
; #define LAS __attribute__((address_space(3)))
; __device__ __forceinline__ unsigned pk2(float lo, float hi) { return f2bf(lo) | (f2bf(hi) << 16); }
; __global__ void __launch_bounds__(NWAVES * 64, 2) trunk_fwd(Args args) {
;     ...
;                     for (int jj = 0; jj < 8; ++jj) { const f32x4 gg = gr[64 * jj]; const float a0 = v[jj].x * rstd * gg.x, a1 = v[jj].y * rstd * gg.y, a2 = v[jj].z * rstd * gg.z, a3 = v[jj].w * rstd * gg.w;
;                         o8[64 * jj] = (unsigned long long)pk2(a0, a1) | ((unsigned long long)pk2(a2, a3) << 32);
;                         const int c0 = 256 * jj + 4 * lane; const float av[4] = {a0, a1, a2, a3};
; #pragma unroll
;                         for (int q = 0; q < 4; ++q) { const f32x4 w0 = *(const LAS f32x4*)(RW + (c0 + q) * 8), w1 = *(const LAS f32x4*)(RW + (c0 + q) * 8 + 4);
;                             lg[0] += av[q] * w0.x; lg[1] += av[q] * w0.y; lg[2] += av[q] * w0.z; lg[3] += av[q] * w0.w; lg[4] += av[q] * w1.x; lg[5] += av[q] * w1.y; lg[6] += av[q] * w1.z; lg[7] += av[q] * w1.w; } }
	v_fmac_f32_e32 v77, v64, v82
	v_fmac_f32_e32 v76, v64, v83
	v_fmac_f32_e32 v75, v64, v84
	v_fmac_f32_e32 v74, v64, v85
	ds_read_b128 v[38:41], v73 offset:96
	ds_read_b128 v[82:85], v73 offset:112
	s_waitcnt lgkmcnt(1)
	v_fmac_f32_e32 v79, v66, v40
	s_waitcnt lgkmcnt(0)
	v_fmac_f32_e32 v77, v66, v82
	v_fmac_f32_e32 v76, v66, v83
	v_fmac_f32_e32 v75, v66, v84
	v_fmac_f32_e32 v74, v66, v85
	v_fmac_f32_e32 v78, v66, v41
	v_mul_f32_e32 v72, v26, v104
	v_mul_f32_e32 v26, v80, v27
	v_mul_f32_e32 v40, v26, v105
	v_mul_f32_e32 v26, v80, v28
	v_mul_f32_e32 v68, v26, v106
	v_mul_f32_e32 v26, v80, v29
	v_mul_f32_e32 v70, v26, v107
	v_bfe_u32 v26, v72, 16, 1
	v_add3_u32 v26, v72, v26, s36
	v_bfe_u32 v27, v40, 16, 1
	v_lshrrev_b32_e32 v26, 16, v26
	v_add3_u32 v27, v40, v27, s36
	v_and_or_b32 v26, v27, s27, v26
	v_bfe_u32 v27, v68, 16, 1
	v_add3_u32 v27, v68, v27, s36
	v_bfe_u32 v28, v70, 16, 1
	v_lshrrev_b32_e32 v27, 16, v27
	v_add3_u32 v28, v70, v28, s36
	v_and_or_b32 v27, v28, s27, v27
	global_store_dwordx2 v[58:59], v[26:27], off offset:512
	v_pk_fma_f32 v[26:27], v[60:61], v[30:31], 0 op_sel_hi:[0,1,0]
	v_pk_fma_f32 v[26:27], v[62:63], v[34:35], v[26:27] op_sel_hi:[0,1,1]
	v_pk_fma_f32 v[26:27], v[64:65], v[36:37], v[26:27] op_sel_hi:[0,1,1]
	v_pk_fma_f32 v[38:39], v[66:67], v[38:39], v[26:27] op_sel_hi:[0,1,1]
	ds_read_b128 v[30:33], v73 offset:8192
	ds_read_b128 v[34:37], v73 offset:8208
	ds_read_b128 v[26:29], v73 offset:8224
	ds_read_b128 v[82:85], v73 offset:8240
	s_waitcnt lgkmcnt(3)
	v_fmac_f32_e32 v79, v72, v32
	v_fmac_f32_e32 v78, v72, v33
	v_pk_fma_f32 v[60:61], v[72:73], v[30:31], v[38:39] op_sel_hi:[0,1,1]
	s_waitcnt lgkmcnt(2)
	v_fmac_f32_e32 v77, v72, v34
	v_fmac_f32_e32 v76, v72, v35
	s_waitcnt lgkmcnt(1)
	v_fmac_f32_e32 v79, v40, v28
	v_fmac_f32_e32 v78, v40, v29
	ds_read_b128 v[28:31], v73 offset:8256
	ds_read_b128 v[32:35], v73 offset:8272
	v_fmac_f32_e32 v75, v72, v36
	v_fmac_f32_e32 v74, v72, v37
	s_waitcnt lgkmcnt(2)
	v_fmac_f32_e32 v77, v40, v82
	v_fmac_f32_e32 v76, v40, v83
	v_fmac_f32_e32 v75, v40, v84
	v_fmac_f32_e32 v74, v40, v85
	s_waitcnt lgkmcnt(1)
	v_fmac_f32_e32 v79, v68, v30
	v_fmac_f32_e32 v78, v68, v31
	s_waitcnt lgkmcnt(0)
	v_fmac_f32_e32 v77, v68, v32
	v_fmac_f32_e32 v76, v68, v33
	v_fmac_f32_e32 v75, v68, v34
	v_fmac_f32_e32 v74, v68, v35
	ds_read_b128 v[30:33], v73 offset:8288
	ds_read_b128 v[34:37], v73 offset:8304
	s_waitcnt lgkmcnt(1)
	v_fmac_f32_e32 v79, v70, v32
	v_fmac_f32_e32 v78, v70, v33
	s_waitcnt lgkmcnt(0)
	v_fmac_f32_e32 v77, v70, v34
	v_fmac_f32_e32 v76, v70, v35
	v_fmac_f32_e32 v75, v70, v36
	v_fmac_f32_e32 v74, v70, v37
	v_mul_f32_e32 v62, v22, v108
	v_mul_f32_e32 v22, v80, v23
	v_mul_f32_e32 v64, v22, v109
	v_mul_f32_e32 v22, v80, v24
	v_mul_f32_e32 v66, v22, v110
	v_mul_f32_e32 v22, v80, v25
	v_mul_f32_e32 v72, v22, v111
	v_bfe_u32 v22, v62, 16, 1
	v_add3_u32 v22, v62, v22, s36
	v_bfe_u32 v23, v64, 16, 1
	v_lshrrev_b32_e32 v22, 16, v22
	v_add3_u32 v23, v64, v23, s36
	v_and_or_b32 v22, v23, s27, v22
	v_bfe_u32 v23, v66, 16, 1
	v_add3_u32 v23, v66, v23, s36
	v_bfe_u32 v24, v72, 16, 1
	v_lshrrev_b32_e32 v23, 16, v23
	v_add3_u32 v24, v72, v24, s36
	v_and_or_b32 v23, v24, s27, v23
	global_store_dwordx2 v[58:59], v[22:23], off offset:1024
	ds_read_b128 v[22:25], v73 offset:16384
	ds_read_b128 v[36:39], v73 offset:16400
	ds_read_b128 v[32:35], v73 offset:16416
	ds_read_b128 v[82:85], v73 offset:16432
	s_waitcnt lgkmcnt(3)
	v_fmac_f32_e32 v79, v62, v24
	v_fmac_f32_e32 v78, v62, v25
	s_waitcnt lgkmcnt(2)
	v_fmac_f32_e32 v77, v62, v36
	v_fmac_f32_e32 v76, v62, v37
	v_fmac_f32_e32 v75, v62, v38
	v_fmac_f32_e32 v74, v62, v39
	s_waitcnt lgkmcnt(1)
	v_fmac_f32_e32 v79, v64, v34
	v_fmac_f32_e32 v78, v64, v35
	s_waitcnt lgkmcnt(0)
	v_fmac_f32_e32 v77, v64, v82
	v_fmac_f32_e32 v76, v64, v83
	v_fmac_f32_e32 v75, v64, v84
	v_fmac_f32_e32 v74, v64, v85
	ds_read_b128 v[34:37], v73 offset:16448
	ds_read_b128 v[82:85], v73 offset:16464
	s_waitcnt lgkmcnt(1)
	v_fmac_f32_e32 v79, v66, v36
	v_fmac_f32_e32 v78, v66, v37
	s_waitcnt lgkmcnt(0)
	v_fmac_f32_e32 v77, v66, v82
	v_fmac_f32_e32 v76, v66, v83
	v_fmac_f32_e32 v75, v66, v84
	v_fmac_f32_e32 v74, v66, v85
	ds_read_b128 v[36:39], v73 offset:16480
	ds_read_b128 v[82:85], v73 offset:16496
	s_waitcnt lgkmcnt(1)
	v_fmac_f32_e32 v79, v72, v38
	s_waitcnt lgkmcnt(0)
	v_fmac_f32_e32 v77, v72, v82
	v_fmac_f32_e32 v76, v72, v83
	v_fmac_f32_e32 v75, v72, v84
	v_fmac_f32_e32 v74, v72, v85
	v_fmac_f32_e32 v78, v72, v39
	v_mul_f32_e32 v24, v18, v112
	v_mul_f32_e32 v18, v80, v19
	v_mul_f32_e32 v38, v18, v113
	v_mul_f32_e32 v18, v80, v20
	v_mul_f32_e32 v96, v18, v114
	v_mul_f32_e32 v18, v80, v21
	v_mul_f32_e32 v98, v18, v115
	v_bfe_u32 v18, v24, 16, 1
	v_add3_u32 v18, v24, v18, s36
	v_bfe_u32 v19, v38, 16, 1
	v_lshrrev_b32_e32 v18, 16, v18
	v_add3_u32 v19, v38, v19, s36
	v_and_or_b32 v18, v19, s27, v18
	v_bfe_u32 v19, v96, 16, 1
	v_add3_u32 v19, v96, v19, s36
	v_bfe_u32 v20, v98, 16, 1
	v_lshrrev_b32_e32 v19, 16, v19
	v_add3_u32 v20, v98, v20, s36
	v_and_or_b32 v19, v20, s27, v19
	global_store_dwordx2 v[58:59], v[18:19], off offset:1536
	ds_read_b128 v[18:21], v73 offset:24576
	ds_read_b128 v[82:85], v73 offset:24592
	ds_read_b128 v[86:89], v73 offset:24608
	ds_read_b128 v[90:93], v73 offset:24624
	s_waitcnt lgkmcnt(3)
	v_fmac_f32_e32 v79, v24, v20
	v_fmac_f32_e32 v78, v24, v21
	s_waitcnt lgkmcnt(2)
	v_fmac_f32_e32 v77, v24, v82
	v_fmac_f32_e32 v76, v24, v83
	v_pk_fma_f32 v[20:21], v[40:41], v[26:27], v[60:61] op_sel_hi:[0,1,1]
	v_fmac_f32_e32 v75, v24, v84
	v_fmac_f32_e32 v74, v24, v85
	s_waitcnt lgkmcnt(1)
	v_fmac_f32_e32 v79, v38, v88
	v_fmac_f32_e32 v78, v38, v89
	s_waitcnt lgkmcnt(0)
; #define LAS __attribute__((address_space(3)))
; __device__ __forceinline__ unsigned pk2(float lo, float hi) { return f2bf(lo) | (f2bf(hi) << 16); }
; __global__ void __launch_bounds__(NWAVES * 64, 2) trunk_fwd(Args args) {
;     ...
;                     for (int jj = 0; jj < 8; ++jj) { const f32x4 gg = gr[64 * jj]; const float a0 = v[jj].x * rstd * gg.x, a1 = v[jj].y * rstd * gg.y, a2 = v[jj].z * rstd * gg.z, a3 = v[jj].w * rstd * gg.w;
;                         o8[64 * jj] = (unsigned long long)pk2(a0, a1) | ((unsigned long long)pk2(a2, a3) << 32);
;                         const int c0 = 256 * jj + 4 * lane; const float av[4] = {a0, a1, a2, a3};
; #pragma unroll
;                         for (int q = 0; q < 4; ++q) { const f32x4 w0 = *(const LAS f32x4*)(RW + (c0 + q) * 8), w1 = *(const LAS f32x4*)(RW + (c0 + q) * 8 + 4);
;                             lg[0] += av[q] * w0.x; lg[1] += av[q] * w0.y; lg[2] += av[q] * w0.z; lg[3] += av[q] * w0.w; lg[4] += av[q] * w1.x; lg[5] += av[q] * w1.y; lg[6] += av[q] * w1.z; lg[7] += av[q] * w1.w; } }
	v_fmac_f32_e32 v77, v38, v90
	v_fmac_f32_e32 v76, v38, v91
	ds_read_b128 v[82:85], v73 offset:24640
	ds_read_b128 v[88:91], v73 offset:24656
	v_pk_fma_f32 v[20:21], v[68:69], v[28:29], v[20:21] op_sel_hi:[0,1,1]
	v_pk_fma_f32 v[20:21], v[70:71], v[30:31], v[20:21] op_sel_hi:[0,1,1]
	v_pk_fma_f32 v[20:21], v[62:63], v[22:23], v[20:21] op_sel_hi:[0,1,1]
	v_pk_fma_f32 v[20:21], v[64:65], v[32:33], v[20:21] op_sel_hi:[0,1,1]
	v_fmac_f32_e32 v75, v38, v92
	v_fmac_f32_e32 v74, v38, v93
	v_pk_fma_f32 v[20:21], v[66:67], v[34:35], v[20:21] op_sel_hi:[0,1,1]
	s_waitcnt lgkmcnt(0)
	v_fmac_f32_e32 v77, v96, v88
	v_fmac_f32_e32 v76, v96, v89
	v_fmac_f32_e32 v75, v96, v90
	v_fmac_f32_e32 v74, v96, v91
	ds_read_b128 v[88:91], v73 offset:24672
	ds_read_b128 v[92:95], v73 offset:24688
	v_pk_fma_f32 v[20:21], v[72:73], v[36:37], v[20:21] op_sel_hi:[0,1,1]
	v_pk_fma_f32 v[18:19], v[24:25], v[18:19], v[20:21] op_sel_hi:[0,1,1]
	v_pk_fma_f32 v[18:19], v[38:39], v[86:87], v[18:19] op_sel_hi:[0,1,1]
	v_pk_fma_f32 v[18:19], v[96:97], v[82:83], v[18:19] op_sel_hi:[0,1,1]
	s_waitcnt lgkmcnt(1)
	v_pk_fma_f32 v[32:33], v[98:99], v[88:89], v[18:19] op_sel_hi:[0,1,1]
	v_fmac_f32_e32 v79, v96, v84
	v_fmac_f32_e32 v78, v96, v85
	v_fmac_f32_e32 v79, v98, v90
	v_fmac_f32_e32 v78, v98, v91
	s_waitcnt lgkmcnt(0)
	v_fmac_f32_e32 v77, v98, v92
	v_fmac_f32_e32 v76, v98, v93
	v_fmac_f32_e32 v75, v98, v94
	v_fmac_f32_e32 v74, v98, v95
	v_mul_f32_e32 v34, v14, v116
	v_mul_f32_e32 v14, v80, v15
	v_mul_f32_e32 v36, v14, v117
	v_mul_f32_e32 v14, v80, v16
	v_mul_f32_e32 v38, v14, v118
	v_mul_f32_e32 v14, v80, v17
	v_mul_f32_e32 v40, v14, v119
	v_bfe_u32 v14, v34, 16, 1
	v_add3_u32 v14, v34, v14, s36
	v_bfe_u32 v15, v36, 16, 1
	v_lshrrev_b32_e32 v14, 16, v14
	v_add3_u32 v15, v36, v15, s36
	v_and_or_b32 v14, v15, s27, v14
	v_bfe_u32 v15, v38, 16, 1
	v_add3_u32 v15, v38, v15, s36
	v_bfe_u32 v16, v40, 16, 1
	v_lshrrev_b32_e32 v15, 16, v15
	v_add3_u32 v16, v40, v16, s36
	v_and_or_b32 v15, v16, s27, v15
	global_store_dwordx2 v[58:59], v[14:15], off offset:2048
	ds_read_b128 v[14:17], v73 offset:32768
	ds_read_b128 v[22:25], v73 offset:32784
	ds_read_b128 v[18:21], v73 offset:32800
	ds_read_b128 v[26:29], v73 offset:32816
	s_waitcnt lgkmcnt(3)
	v_fmac_f32_e32 v79, v34, v16
	v_fmac_f32_e32 v78, v34, v17
	s_waitcnt lgkmcnt(2)
	v_fmac_f32_e32 v77, v34, v22
	v_fmac_f32_e32 v76, v34, v23
	v_fmac_f32_e32 v75, v34, v24
	v_fmac_f32_e32 v74, v34, v25
	s_waitcnt lgkmcnt(1)
	v_fmac_f32_e32 v79, v36, v20
	v_fmac_f32_e32 v78, v36, v21
	s_waitcnt lgkmcnt(0)
	v_fmac_f32_e32 v77, v36, v26
	v_fmac_f32_e32 v76, v36, v27
	ds_read_b128 v[20:23], v73 offset:32832
	ds_read_b128 v[24:27], v73 offset:32848
	v_fmac_f32_e32 v75, v36, v28
	v_fmac_f32_e32 v74, v36, v29
	s_waitcnt lgkmcnt(1)
	v_fmac_f32_e32 v79, v38, v22
	v_fmac_f32_e32 v78, v38, v23
	s_waitcnt lgkmcnt(0)
	v_fmac_f32_e32 v77, v38, v24
	v_fmac_f32_e32 v76, v38, v25
	v_fmac_f32_e32 v75, v38, v26
	v_fmac_f32_e32 v74, v38, v27
	ds_read_b128 v[22:25], v73 offset:32864
	ds_read_b128 v[26:29], v73 offset:32880
	s_waitcnt lgkmcnt(1)
	v_fmac_f32_e32 v79, v40, v24
	v_fmac_f32_e32 v78, v40, v25
	s_waitcnt lgkmcnt(0)
	v_fmac_f32_e32 v77, v40, v26
	v_fmac_f32_e32 v76, v40, v27
	v_fmac_f32_e32 v75, v40, v28
	v_fmac_f32_e32 v74, v40, v29
	v_mul_f32_e32 v60, v10, v120
	v_mul_f32_e32 v10, v80, v11
	v_mul_f32_e32 v62, v10, v121
	v_mul_f32_e32 v10, v80, v12
	v_mul_f32_e32 v64, v10, v122
	v_mul_f32_e32 v10, v80, v13
	v_mul_f32_e32 v66, v10, v123
	v_bfe_u32 v10, v60, 16, 1
	v_add3_u32 v10, v60, v10, s36
	v_bfe_u32 v11, v62, 16, 1
	v_lshrrev_b32_e32 v10, 16, v10
	v_add3_u32 v11, v62, v11, s36
	v_and_or_b32 v10, v11, s27, v10
	v_bfe_u32 v11, v64, 16, 1
	v_add3_u32 v11, v64, v11, s36
	v_bfe_u32 v12, v66, 16, 1
	v_lshrrev_b32_e32 v11, 16, v11
	v_add3_u32 v12, v66, v12, s36
	v_and_or_b32 v11, v12, s27, v11
	global_store_dwordx2 v[58:59], v[10:11], off offset:2560
	ds_read_b128 v[10:13], v73 offset:40960
	ds_read_b128 v[28:31], v73 offset:40976
	ds_read_b128 v[24:27], v73 offset:40992
	ds_read_b128 v[82:85], v73 offset:41008
	s_waitcnt lgkmcnt(3)
	v_fmac_f32_e32 v79, v60, v12
	v_fmac_f32_e32 v78, v60, v13
	s_waitcnt lgkmcnt(2)
	v_fmac_f32_e32 v77, v60, v28
	v_fmac_f32_e32 v76, v60, v29
	v_fmac_f32_e32 v75, v60, v30
	v_fmac_f32_e32 v74, v60, v31
	s_waitcnt lgkmcnt(1)
	v_fmac_f32_e32 v79, v62, v26
	v_fmac_f32_e32 v78, v62, v27
	s_waitcnt lgkmcnt(0)
	v_fmac_f32_e32 v77, v62, v82
	v_fmac_f32_e32 v76, v62, v83
	v_fmac_f32_e32 v75, v62, v84
	v_fmac_f32_e32 v74, v62, v85
	ds_read_b128 v[26:29], v73 offset:41024
	ds_read_b128 v[82:85], v73 offset:41040
	s_waitcnt lgkmcnt(1)
	v_fmac_f32_e32 v79, v64, v28
	v_fmac_f32_e32 v78, v64, v29
	s_waitcnt lgkmcnt(0)
	v_fmac_f32_e32 v77, v64, v82
	v_fmac_f32_e32 v76, v64, v83
	v_fmac_f32_e32 v75, v64, v84
	v_fmac_f32_e32 v74, v64, v85
	ds_read_b128 v[28:31], v73 offset:41056
	ds_read_b128 v[82:85], v73 offset:41072
	s_waitcnt lgkmcnt(1)
	v_fmac_f32_e32 v79, v66, v30
	s_waitcnt lgkmcnt(0)
	v_fmac_f32_e32 v77, v66, v82
	v_fmac_f32_e32 v76, v66, v83
	v_fmac_f32_e32 v75, v66, v84
	v_fmac_f32_e32 v74, v66, v85
	v_fmac_f32_e32 v78, v66, v31
	v_mul_f32_e32 v12, v6, v124
	v_mul_f32_e32 v6, v80, v7
	v_mul_f32_e32 v7, v80, v9
	v_mul_f32_e32 v30, v6, v125
	v_mul_f32_e32 v16, v7, v127
	v_bfe_u32 v7, v12, 16, 1
	v_mul_f32_e32 v6, v80, v8
	v_add3_u32 v7, v12, v7, s36
	v_bfe_u32 v8, v30, 16, 1
	v_mul_f32_e32 v6, v6, v126
	v_lshrrev_b32_e32 v7, 16, v7
	v_add3_u32 v8, v30, v8, s36
	v_and_or_b32 v8, v8, s27, v7
	v_bfe_u32 v7, v6, 16, 1
	v_add3_u32 v7, v6, v7, s36
	v_bfe_u32 v9, v16, 16, 1
	v_lshrrev_b32_e32 v7, 16, v7
	v_add3_u32 v9, v16, v9, s36
	v_and_or_b32 v9, v9, s27, v7
	global_store_dwordx2 v[58:59], v[8:9], off offset:3072
	ds_read_b128 v[82:85], v73 offset:49152
	ds_read_b128 v[86:89], v73 offset:49168
	ds_read_b128 v[90:93], v73 offset:49184
	ds_read_b128 v[94:97], v73 offset:49200
	v_pk_fma_f32 v[8:9], v[34:35], v[14:15], v[32:33] op_sel_hi:[0,1,1]
	v_pk_fma_f32 v[8:9], v[36:37], v[18:19], v[8:9] op_sel_hi:[0,1,1]
	v_pk_fma_f32 v[8:9], v[38:39], v[20:21], v[8:9] op_sel_hi:[0,1,1]
	v_pk_fma_f32 v[8:9], v[40:41], v[22:23], v[8:9] op_sel_hi:[0,1,1]
	s_waitcnt lgkmcnt(3)
; #define LAS __attribute__((address_space(3)))
; __device__ __forceinline__ float wave_sum(float v) {
; #pragma unroll
;     for (int o = 1; o < 64; o <<= 1) v += __shfl_xor(v, o);
;     return v;
; __global__ void __launch_bounds__(NWAVES * 64, 2) trunk_fwd(Args args) {
;     ...
;                         for (int q = 0; q < 4; ++q) { const f32x4 w0 = *(const LAS f32x4*)(RW + (c0 + q) * 8), w1 = *(const LAS f32x4*)(RW + (c0 + q) * 8 + 4);
;                             lg[0] += av[q] * w0.x; lg[1] += av[q] * w0.y; lg[2] += av[q] * w0.z; lg[3] += av[q] * w0.w; lg[4] += av[q] * w1.x; lg[5] += av[q] * w1.y; lg[6] += av[q] * w1.z; lg[7] += av[q] * w1.w; } }
; #pragma unroll
;                     for (int e = 0; e < 8; ++e) lg[e] = wave_sum(lg[e]) + args.in[I_RB][e];
	v_fmac_f32_e32 v79, v12, v84
	v_fmac_f32_e32 v78, v12, v85
	s_waitcnt lgkmcnt(2)
	v_fmac_f32_e32 v77, v12, v86
	v_fmac_f32_e32 v76, v12, v87
	v_pk_fma_f32 v[8:9], v[60:61], v[10:11], v[8:9] op_sel_hi:[0,1,1]
	s_waitcnt lgkmcnt(1)
	v_fmac_f32_e32 v79, v30, v92
	v_fmac_f32_e32 v78, v30, v93
	s_waitcnt lgkmcnt(0)
	v_fmac_f32_e32 v77, v30, v94
	v_fmac_f32_e32 v76, v30, v95
	ds_read_b128 v[84:87], v73 offset:49216
	ds_read_b128 v[92:95], v73 offset:49232
	v_pk_fma_f32 v[8:9], v[62:63], v[24:25], v[8:9] op_sel_hi:[0,1,1]
	v_pk_fma_f32 v[8:9], v[64:65], v[26:27], v[8:9] op_sel_hi:[0,1,1]
	v_pk_fma_f32 v[8:9], v[66:67], v[28:29], v[8:9] op_sel_hi:[0,1,1]
	v_fmac_f32_e32 v75, v12, v88
	v_fmac_f32_e32 v74, v12, v89
	v_pk_fma_f32 v[8:9], v[12:13], v[82:83], v[8:9] op_sel_hi:[0,1,1]
	v_fmac_f32_e32 v75, v30, v96
	v_fmac_f32_e32 v74, v30, v97
	v_pk_fma_f32 v[8:9], v[30:31], v[90:91], v[8:9] op_sel_hi:[0,1,1]
	s_waitcnt lgkmcnt(1)
	v_pk_fma_f32 v[18:19], v[6:7], v[84:85], v[8:9] op_sel_hi:[0,1,1]
	v_fmac_f32_e32 v79, v6, v86
	v_fmac_f32_e32 v78, v6, v87
	s_waitcnt lgkmcnt(0)
	v_fmac_f32_e32 v77, v6, v92
	v_fmac_f32_e32 v76, v6, v93
	v_fmac_f32_e32 v75, v6, v94
	v_fmac_f32_e32 v74, v6, v95
	ds_read_b128 v[6:9], v73 offset:49248
	ds_read_b128 v[10:13], v73 offset:49264
	s_waitcnt lgkmcnt(1)
	v_fmac_f32_e32 v79, v16, v8
	v_fmac_f32_e32 v78, v16, v9
	s_waitcnt lgkmcnt(0)
	v_fmac_f32_e32 v77, v16, v10
	v_fmac_f32_e32 v76, v16, v11
	v_fmac_f32_e32 v75, v16, v12
	v_fmac_f32_e32 v74, v16, v13
	v_mul_f32_e32 v24, v2, v128
	v_mul_f32_e32 v2, v80, v3
	v_mul_f32_e32 v26, v2, v129
	v_mul_f32_e32 v2, v80, v4
	v_mul_f32_e32 v22, v2, v130
	v_mul_f32_e32 v2, v80, v5
	v_mul_f32_e32 v20, v2, v131
	v_bfe_u32 v2, v24, 16, 1
	v_add3_u32 v2, v24, v2, s36
	v_bfe_u32 v3, v26, 16, 1
	v_lshrrev_b32_e32 v2, 16, v2
	v_add3_u32 v3, v26, v3, s36
	v_and_or_b32 v2, v3, s27, v2
	v_bfe_u32 v3, v22, 16, 1
	v_add3_u32 v3, v22, v3, s36
	v_bfe_u32 v4, v20, 16, 1
	v_lshrrev_b32_e32 v3, 16, v3
	v_add3_u32 v4, v20, v4, s36
	v_and_or_b32 v3, v4, s27, v3
	global_store_dwordx2 v[58:59], v[2:3], off offset:3584
	ds_read_b128 v[8:11], v73 offset:57344
	ds_read_b128 v[12:15], v73 offset:57360
	ds_read_b128 v[2:5], v73 offset:57376
	ds_read_b128 v[28:31], v73 offset:57392
	s_waitcnt lgkmcnt(3)
	v_fmac_f32_e32 v79, v24, v10
	s_waitcnt lgkmcnt(2)
	v_fmac_f32_e32 v77, v24, v12
	v_fmac_f32_e32 v76, v24, v13
	v_fmac_f32_e32 v75, v24, v14
	v_fmac_f32_e32 v74, v24, v15
	v_fmac_f32_e32 v78, v24, v11
	s_waitcnt lgkmcnt(0)
	v_fmac_f32_e32 v77, v26, v28
	v_fmac_f32_e32 v76, v26, v29
	v_fmac_f32_e32 v75, v26, v30
	v_fmac_f32_e32 v74, v26, v31
	ds_read_b128 v[10:13], v73 offset:57408
	ds_read_b128 v[28:31], v73 offset:57424
	v_fmac_f32_e32 v79, v26, v4
	v_fmac_f32_e32 v78, v26, v5
	v_pk_fma_f32 v[4:5], v[16:17], v[6:7], v[18:19] op_sel_hi:[0,1,1]
	s_waitcnt lgkmcnt(1)
	v_fmac_f32_e32 v79, v22, v12
	v_fmac_f32_e32 v78, v22, v13
	s_waitcnt lgkmcnt(0)
	v_fmac_f32_e32 v77, v22, v28
	v_fmac_f32_e32 v76, v22, v29
	v_fmac_f32_e32 v75, v22, v30
	v_fmac_f32_e32 v74, v22, v31
	ds_read_b128 v[12:15], v73 offset:57440
	ds_read_b128 v[28:31], v73 offset:57456
	v_pk_fma_f32 v[4:5], v[24:25], v[8:9], v[4:5] op_sel_hi:[0,1,1]
	v_pk_fma_f32 v[2:3], v[26:27], v[2:3], v[4:5] op_sel_hi:[0,1,1]
	v_pk_fma_f32 v[2:3], v[22:23], v[10:11], v[2:3] op_sel_hi:[0,1,1]
	s_waitcnt lgkmcnt(1)
	v_fmac_f32_e32 v78, v20, v15
	ds_bpermute_b32 v8, v43, v78
	s_waitcnt lgkmcnt(1)
	v_fmac_f32_e32 v77, v20, v28
	v_fmac_f32_e32 v76, v20, v29
	v_pk_fma_f32 v[2:3], v[20:21], v[12:13], v[2:3] op_sel_hi:[0,1,1]
	v_fmac_f32_e32 v75, v20, v30
	s_waitcnt lgkmcnt(0)
	v_add_f32_e32 v8, v78, v8
	ds_bpermute_b32 v9, v63, v8
	v_fmac_f32_e32 v79, v20, v14
	v_fmac_f32_e32 v74, v20, v31
	ds_bpermute_b32 v4, v43, v2
	ds_bpermute_b32 v5, v43, v3
	s_waitcnt lgkmcnt(2)
	v_add_f32_e32 v8, v8, v9
	ds_bpermute_b32 v9, v65, v8
	ds_bpermute_b32 v6, v43, v79
	s_waitcnt lgkmcnt(2)
	v_pk_add_f32 v[2:3], v[2:3], v[4:5]
	ds_bpermute_b32 v4, v63, v2
	s_waitcnt lgkmcnt(2)
	v_add_f32_e32 v8, v8, v9
	ds_bpermute_b32 v9, v67, v8
	s_waitcnt lgkmcnt(2)
	v_add_f32_e32 v6, v79, v6
	ds_bpermute_b32 v5, v63, v3
	ds_bpermute_b32 v7, v63, v6
	s_waitcnt lgkmcnt(2)
	v_add_f32_e32 v8, v8, v9
	ds_bpermute_b32 v9, v69, v8
	s_waitcnt lgkmcnt(2)
	v_pk_add_f32 v[2:3], v[2:3], v[4:5]
	s_waitcnt lgkmcnt(1)
	v_add_f32_e32 v6, v6, v7
	ds_bpermute_b32 v4, v65, v2
	ds_bpermute_b32 v5, v65, v3
	s_waitcnt lgkmcnt(2)
	v_add_f32_e32 v9, v8, v9
	ds_bpermute_b32 v8, v43, v77
	ds_bpermute_b32 v7, v65, v6
	ds_bpermute_b32 v10, v71, v9
	s_waitcnt lgkmcnt(3)
	v_pk_add_f32 v[2:3], v[2:3], v[4:5]
	ds_bpermute_b32 v4, v67, v2
	s_waitcnt lgkmcnt(3)
	v_add_f32_e32 v8, v77, v8
	ds_bpermute_b32 v11, v63, v8
	s_waitcnt lgkmcnt(3)
	v_add_f32_e32 v6, v6, v7
	ds_bpermute_b32 v5, v67, v3
	ds_bpermute_b32 v7, v67, v6
	s_waitcnt lgkmcnt(2)
	v_add_f32_e32 v8, v8, v11
	ds_bpermute_b32 v11, v65, v8
	s_waitcnt lgkmcnt(2)
	v_pk_add_f32 v[2:3], v[2:3], v[4:5]
	s_waitcnt lgkmcnt(1)
	v_add_f32_e32 v6, v6, v7
	ds_bpermute_b32 v4, v69, v2
	ds_bpermute_b32 v5, v69, v3
	s_waitcnt lgkmcnt(2)
	v_add_f32_e32 v8, v8, v11
	ds_bpermute_b32 v11, v67, v8
	ds_bpermute_b32 v7, v69, v6
	s_waitcnt lgkmcnt(2)
	v_pk_add_f32 v[2:3], v[2:3], v[4:5]
	ds_bpermute_b32 v4, v71, v2
	s_waitcnt lgkmcnt(2)
	v_add_f32_e32 v8, v8, v11
	ds_bpermute_b32 v11, v69, v8
	s_waitcnt lgkmcnt(2)
	v_add_f32_e32 v6, v6, v7
	ds_bpermute_b32 v5, v71, v3
	ds_bpermute_b32 v7, v71, v6
	s_waitcnt lgkmcnt(2)
	v_add_f32_e32 v12, v8, v11
	ds_bpermute_b32 v8, v43, v76
	ds_bpermute_b32 v13, v71, v12
	s_waitcnt lgkmcnt(1)
	v_add_f32_e32 v8, v76, v8
	ds_bpermute_b32 v11, v63, v8
	s_waitcnt lgkmcnt(0)
	v_add_f32_e32 v8, v8, v11
	ds_bpermute_b32 v11, v65, v8
	s_waitcnt lgkmcnt(0)
	v_add_f32_e32 v8, v8, v11
	ds_bpermute_b32 v11, v67, v8
	s_waitcnt lgkmcnt(0)
	v_add_f32_e32 v8, v8, v11
	ds_bpermute_b32 v11, v69, v8
	s_waitcnt lgkmcnt(0)
	v_add_f32_e32 v14, v8, v11
	ds_bpermute_b32 v8, v43, v75
	ds_bpermute_b32 v15, v71, v14
	s_waitcnt lgkmcnt(1)
	v_add_f32_e32 v8, v75, v8
	ds_bpermute_b32 v11, v63, v8
	s_waitcnt lgkmcnt(0)
	v_add_f32_e32 v8, v8, v11
	ds_bpermute_b32 v11, v65, v8
	s_waitcnt lgkmcnt(0)
	v_add_f32_e32 v8, v8, v11
	ds_bpermute_b32 v11, v67, v8
	s_waitcnt lgkmcnt(0)
	v_add_f32_e32 v8, v8, v11
	ds_bpermute_b32 v11, v69, v8
	s_waitcnt lgkmcnt(0)
	v_add_f32_e32 v11, v8, v11
	ds_bpermute_b32 v8, v43, v74
	ds_bpermute_b32 v16, v71, v11
	s_waitcnt lgkmcnt(1)
	v_add_f32_e32 v8, v74, v8
	ds_bpermute_b32 v17, v63, v8
	s_waitcnt lgkmcnt(0)
	v_add_f32_e32 v8, v8, v17
	ds_bpermute_b32 v17, v65, v8
	s_waitcnt lgkmcnt(0)
	v_add_f32_e32 v8, v8, v17
	ds_bpermute_b32 v17, v67, v8
	s_waitcnt lgkmcnt(0)
	v_add_f32_e32 v8, v8, v17
	ds_bpermute_b32 v17, v69, v8
	s_waitcnt lgkmcnt(0)
	v_add_f32_e32 v8, v8, v17
	ds_bpermute_b32 v17, v71, v8
	s_and_saveexec_b64 s[20:21], s[42:43]
	s_cbranch_execz .LBB0_769
; __global__ void __launch_bounds__(NWAVES * 64, 2) trunk_fwd(Args args) {
;     ...
;                     for (int e = 0; e < 8; ++e) lg[e] = wave_sum(lg[e]) + args.in[I_RB][e];
;                     if (lane == 0) { int e0 = 0; float v0 = lg[0];
; #pragma unroll
;                         for (int e = 1; e < 8; ++e) if (lg[e] > v0) { v0 = lg[e]; e0 = e; }
;                         int e1 = -1; float v1 = -INFINITY;
; #pragma unroll
;                         for (int e = 0; e < 8; ++e) if (e != e0 && lg[e] > v1) { v1 = lg[e]; e1 = e; }
	v_readlane_b32 s44, v255, 7
	v_readlane_b32 s46, v255, 9
	v_readlane_b32 s47, v255, 10
	v_add_f32_e32 v6, v6, v7
	v_pk_add_f32 v[2:3], v[2:3], v[4:5]
	v_add_f32_e32 v9, v9, v10
	v_add_f32_e32 v12, v12, v13
	v_add_f32_e32 v14, v14, v15
	global_load_dwordx4 v[18:21], v187, s[46:47] offset:16
	global_load_dwordx4 v[22:25], v187, s[46:47]
	v_add_f32_e32 v11, v11, v16
	s_waitcnt lgkmcnt(0)
	v_add_f32_e32 v8, v8, v17
	s_mov_b32 s8, 0xff800000
	v_readlane_b32 s45, v255, 8
	v_readlane_b32 s48, v255, 11
	v_readlane_b32 s49, v255, 12
	v_readlane_b32 s50, v255, 13
	v_readlane_b32 s51, v255, 14
	s_waitcnt vmcnt(1)
	v_add_f32_e32 v12, v12, v18
	s_waitcnt vmcnt(0)
	v_add_f32_e32 v10, v6, v24
	v_pk_add_f32 v[6:7], v[2:3], v[22:23]
	v_add_f32_e32 v9, v9, v25
	v_cmp_gt_f32_e32 vcc, v7, v6
	v_add_f32_e32 v14, v14, v19
	v_add_f32_e32 v11, v11, v20
	v_cndmask_b32_e32 v2, v6, v7, vcc
	v_cndmask_b32_e64 v3, 0, 1, vcc
	v_cmp_gt_f32_e32 vcc, v10, v2
	v_add_f32_e32 v8, v8, v21
	v_cmp_nlg_f32_e64 s[8:9], s8, v6
	v_cndmask_b32_e32 v2, v2, v10, vcc
	v_cndmask_b32_e64 v3, v3, 2, vcc
	v_cmp_gt_f32_e32 vcc, v9, v2
	s_nop 1
	v_cndmask_b32_e32 v2, v2, v9, vcc
	v_cndmask_b32_e64 v3, v3, 3, vcc
	v_cmp_gt_f32_e32 vcc, v12, v2
	s_nop 1
	v_cndmask_b32_e32 v2, v2, v12, vcc
	v_cndmask_b32_e64 v3, v3, 4, vcc
	v_cmp_gt_f32_e32 vcc, v14, v2
	s_nop 1
	v_cndmask_b32_e32 v2, v2, v14, vcc
	v_cmp_ngt_f32_e64 s[0:1], v11, v2
	v_cndmask_b32_e64 v3, v3, 5, vcc
	s_nop 0
	v_cndmask_b32_e64 v4, v11, v2, s[0:1]
	v_cndmask_b32_e64 v2, 6, v3, s[0:1]
	v_cmp_gt_f32_e64 s[4:5], v8, v4
	v_cmp_ngt_f32_e32 vcc, v8, v4
	s_nop 0
	v_cndmask_b32_e64 v2, v2, 7, s[4:5]
	v_cmp_eq_u32_e64 s[6:7], 0, v2
	s_or_b64 s[6:7], s[6:7], s[8:9]
	s_or_b64 s[4:5], s[4:5], s[0:1]
	v_cndmask_b32_e64 v3, v6, v229, s[6:7]
	v_cndmask_b32_e64 v5, 0, -1, s[6:7]
	v_cmp_ne_u32_e64 s[6:7], 1, v2
	v_cmp_gt_f32_e64 s[8:9], v7, v3
	s_and_b64 s[6:7], s[6:7], s[8:9]
	v_cndmask_b32_e64 v3, v3, v7, s[6:7]
	v_cndmask_b32_e64 v5, v5, 1, s[6:7]
	v_cmp_ne_u32_e64 s[6:7], 2, v2
	v_cmp_gt_f32_e64 s[8:9], v10, v3
	s_and_b64 s[6:7], s[6:7], s[8:9]
	v_cndmask_b32_e64 v3, v3, v10, s[6:7]
	v_cndmask_b32_e64 v5, v5, 2, s[6:7]
	v_cmp_ne_u32_e64 s[6:7], 3, v2
	v_cmp_gt_f32_e64 s[8:9], v9, v3
	s_and_b64 s[6:7], s[6:7], s[8:9]
	v_cndmask_b32_e64 v3, v3, v9, s[6:7]
	v_cndmask_b32_e64 v5, v5, 3, s[6:7]
	v_cmp_ne_u32_e64 s[6:7], 4, v2
	v_cmp_gt_f32_e64 s[8:9], v12, v3
	s_and_b64 s[6:7], s[6:7], s[8:9]
	v_cndmask_b32_e64 v3, v3, v12, s[6:7]
	v_cndmask_b32_e64 v5, v5, 4, s[6:7]
	v_cmp_ne_u32_e64 s[6:7], 5, v2
	v_cmp_gt_f32_e64 s[8:9], v14, v3
	s_and_b64 s[6:7], s[6:7], s[8:9]
	v_cndmask_b32_e64 v3, v3, v14, s[6:7]
	v_cmp_gt_f32_e64 s[0:1], v11, v3
	v_cndmask_b32_e64 v6, v5, 5, s[6:7]
	s_and_b64 s[0:1], s[4:5], s[0:1]
	v_cndmask_b32_e64 v5, v3, v11, s[0:1]
	v_cndmask_b32_e64 v3, v6, 6, s[0:1]
	s_and_saveexec_b64 s[0:1], vcc
	s_cbranch_execz .LBB0_768
	v_cmp_gt_f32_e32 vcc, v8, v5
	s_and_saveexec_b64 s[4:5], vcc
	s_cbranch_execz .LBB0_767
	v_mov_b32_e32 v3, 7
	v_mov_b32_e32 v5, v8
	s_branch .LBB0_767

; __device__ __forceinline__ float rms_row_load(const float* xrow, int lane, f32x4 (&v)[8]) {
;     const f32x4* xr = (const f32x4*)xrow + lane; float s = 0.f;
; #pragma unroll
;     for (int j = 0; j < 8; ++j) { v[j] = xr[64 * j]; s += (v[j].x * v[j].x + v[j].y * v[j].y) + (v[j].z * v[j].z + v[j].w * v[j].w); }
;     return 1.0f / sqrtf(wave_sum(s) * (1.0f / D) + EPS);
.LBB0_780:
	v_lshl_add_u64 v[2:3], s[6:7], 0, v[46:47]
	v_add_co_u32_e32 v4, vcc, 0x36da1000, v2
	s_add_i32 s4, s4, s8
	s_nop 0
	v_addc_co_u32_e32 v5, vcc, 0, v3, vcc
	global_load_dwordx4 v[30:33], v[4:5], off nt
	global_load_dwordx4 v[26:29], v[4:5], off offset:1024 nt
	global_load_dwordx4 v[22:25], v[4:5], off offset:2048 nt
	global_load_dwordx4 v[18:21], v[4:5], off offset:3072 nt
	v_add_co_u32_e32 v2, vcc, s9, v2
	v_lshl_add_u64 v[46:47], v[46:47], 0, s[16:17]
	s_nop 0
	v_addc_co_u32_e32 v3, vcc, 0, v3, vcc
	global_load_dwordx4 v[14:17], v[2:3], off nt
	global_load_dwordx4 v[10:13], v[2:3], off offset:1024 nt
	global_load_dwordx4 v[6:9], v[2:3], off offset:2048 nt
	global_load_dwordx4 v[2:5], v[2:3], off offset:3072 nt
	s_cmpk_gt_i32 s4, 0x1fff
	v_lshl_add_u64 v[48:49], s[6:7], 0, v[44:45]
	v_add_co_u32_e32 v48, vcc, s12, v48
	s_nop 1
	v_addc_co_u32_e32 v49, vcc, 0, v49, vcc
	v_lshl_add_u64 v[44:45], v[44:45], 0, s[14:15]
	s_waitcnt vmcnt(7)
	v_mul_f32_e32 v1, v31, v31
	v_mul_f32_e32 v57, v33, v33
	v_fmac_f32_e32 v1, v30, v30
	v_fmac_f32_e32 v57, v32, v32
	v_add_f32_e32 v1, v1, v57
	s_waitcnt vmcnt(6)
	v_mul_f32_e32 v56, v27, v27
	v_mul_f32_e32 v57, v29, v29
	v_fmac_f32_e32 v56, v26, v26
	v_fmac_f32_e32 v57, v28, v28
	v_add_f32_e32 v56, v56, v57
	v_add_f32_e32 v1, v1, v56
	s_waitcnt vmcnt(5)
	v_mul_f32_e32 v56, v23, v23
	v_mul_f32_e32 v57, v25, v25
	v_fmac_f32_e32 v56, v22, v22
	v_fmac_f32_e32 v57, v24, v24
	v_add_f32_e32 v56, v56, v57
	v_add_f32_e32 v1, v1, v56
	s_waitcnt vmcnt(4)
	v_mul_f32_e32 v56, v19, v19
	v_mul_f32_e32 v57, v21, v21
	v_fmac_f32_e32 v56, v18, v18
	v_fmac_f32_e32 v57, v20, v20
	v_add_f32_e32 v56, v56, v57
	v_add_f32_e32 v1, v1, v56
	s_waitcnt vmcnt(3)
	v_mul_f32_e32 v56, v15, v15
	v_mul_f32_e32 v57, v17, v17
	v_fmac_f32_e32 v56, v14, v14
	v_fmac_f32_e32 v57, v16, v16
	v_add_f32_e32 v56, v56, v57
	v_add_f32_e32 v1, v1, v56
	s_waitcnt vmcnt(2)
	v_mul_f32_e32 v56, v11, v11
	v_mul_f32_e32 v57, v13, v13
	v_fmac_f32_e32 v56, v10, v10
	v_fmac_f32_e32 v57, v12, v12
	v_add_f32_e32 v56, v56, v57
	v_add_f32_e32 v1, v1, v56
	s_waitcnt vmcnt(1)
	v_mul_f32_e32 v56, v7, v7
	v_mul_f32_e32 v57, v9, v9
	v_fmac_f32_e32 v56, v6, v6
	v_fmac_f32_e32 v57, v8, v8
	v_add_f32_e32 v56, v56, v57
	v_add_f32_e32 v1, v1, v56
	s_waitcnt vmcnt(0)
	v_mul_f32_e32 v56, v3, v3
	v_mul_f32_e32 v57, v5, v5
	v_fmac_f32_e32 v56, v2, v2
	v_fmac_f32_e32 v57, v4, v4
	v_add_f32_e32 v56, v56, v57
	v_add_f32_e32 v1, v1, v56
	ds_bpermute_b32 v56, v50, v1
	s_waitcnt lgkmcnt(0)
	v_add_f32_e32 v1, v1, v56
	ds_bpermute_b32 v56, v51, v1
	s_waitcnt lgkmcnt(0)
	v_add_f32_e32 v1, v1, v56
	ds_bpermute_b32 v56, v52, v1
	s_waitcnt lgkmcnt(0)
	v_add_f32_e32 v1, v1, v56
	ds_bpermute_b32 v56, v53, v1
	s_waitcnt lgkmcnt(0)
	v_add_f32_e32 v1, v1, v56
	ds_bpermute_b32 v56, v54, v1
	s_waitcnt lgkmcnt(0)
	v_add_f32_e32 v1, v1, v56
	ds_bpermute_b32 v56, v55, v1
	s_waitcnt lgkmcnt(0)
; __device__ __forceinline__ unsigned pk2(float lo, float hi) { return f2bf(lo) | (f2bf(hi) << 16); }
; __device__ __forceinline__ void rms_row_to_bf16(const float* xrow, const float* gain, bf16* orow, int lane) {
;     f32x4 v[8]; const float rstd = rms_row_load(xrow, lane, v);
;     const f32x4* gr = (const f32x4*)gain + lane; unsigned long long* o8 = (unsigned long long*)orow + lane;
; #pragma unroll
;     for (int j = 0; j < 8; ++j) { const f32x4 g = gr[64 * j]; o8[64 * j] = (unsigned long long)pk2(v[j].x * rstd * g.x, v[j].y * rstd * g.y) | ((unsigned long long)pk2(v[j].z * rstd * g.z, v[j].w * rstd * g.w) << 32); }
	v_add_f32_e32 v1, v1, v56
	v_fmamk_f32 v1, v1, 0x3a000000, v226
	v_cmp_gt_f32_e32 vcc, s5, v1
	v_mul_f32_e32 v92, 0x4f800000, v1
	s_nop 0
	v_cndmask_b32_e32 v1, v1, v92, vcc
	v_sqrt_f32_e32 v92, v1
	s_nop 0
	v_add_u32_e32 v93, -1, v92
	v_fma_f32 v56, -v93, v92, v1
	v_cmp_ge_f32_e64 s[0:1], 0, v56
	v_add_u32_e32 v56, 1, v92
	s_nop 0
	v_cndmask_b32_e64 v93, v92, v93, s[0:1]
	v_fma_f32 v92, -v56, v92, v1
	v_cmp_lt_f32_e64 s[0:1], 0, v92
	s_nop 1
	v_cndmask_b32_e64 v92, v93, v56, s[0:1]
	v_mul_f32_e32 v93, 0x37800000, v92
	v_cndmask_b32_e32 v92, v92, v93, vcc
	v_cmp_class_f32_e32 vcc, v1, v225
	s_nop 1
	v_cndmask_b32_e32 v1, v92, v1, vcc
	v_div_scale_f32 v92, s[0:1], v1, v1, 1.0
	v_rcp_f32_e32 v93, v92
	s_nop 0
	v_fma_f32 v56, -v92, v93, 1.0
	v_fmac_f32_e32 v93, v56, v93
	v_div_scale_f32 v56, vcc, 1.0, v1, 1.0
	v_mul_f32_e32 v57, v56, v93
	v_fma_f32 v58, -v92, v57, v56
	v_fmac_f32_e32 v57, v58, v93
	v_fma_f32 v92, -v92, v57, v56
	v_div_fmas_f32 v92, v92, v93, v57
	v_div_fixup_f32 v1, v92, v1, 1.0
	v_mul_f32_e32 v30, v30, v1
	v_mul_f32_e32 v31, v31, v1
	v_mul_f32_e32 v32, v32, v1
	v_mul_f32_e32 v33, v33, v1
	v_mul_f32_e32 v30, v60, v30
	v_mul_f32_e32 v31, v61, v31
	v_mul_f32_e32 v32, v62, v32
	v_mul_f32_e32 v33, v63, v33
	v_bfe_u32 v56, v30, 16, 1
	v_bfe_u32 v57, v31, 16, 1
	v_bfe_u32 v58, v32, 16, 1
	v_bfe_u32 v59, v33, 16, 1
	v_add3_u32 v30, v30, v56, s36
	v_add3_u32 v31, v31, v57, s36
	v_add3_u32 v32, v32, v58, s36
	v_add3_u32 v33, v33, v59, s36
	v_lshrrev_b32_e32 v30, 16, v30
	v_lshrrev_b32_e32 v32, 16, v32
	v_and_or_b32 v30, v31, s27, v30
	v_and_or_b32 v31, v33, s27, v32
	global_store_dwordx2 v[48:49], v[30:31], off
	v_mul_f32_e32 v26, v26, v1
	v_mul_f32_e32 v27, v27, v1
	v_mul_f32_e32 v28, v28, v1
	v_mul_f32_e32 v29, v29, v1
	v_mul_f32_e32 v26, v64, v26
	v_mul_f32_e32 v27, v65, v27
	v_mul_f32_e32 v28, v66, v28
	v_mul_f32_e32 v29, v67, v29
	v_bfe_u32 v56, v26, 16, 1
	v_bfe_u32 v57, v27, 16, 1
	v_bfe_u32 v58, v28, 16, 1
	v_bfe_u32 v59, v29, 16, 1
	v_add3_u32 v26, v26, v56, s36
	v_add3_u32 v27, v27, v57, s36
	v_add3_u32 v28, v28, v58, s36
	v_add3_u32 v29, v29, v59, s36
	v_lshrrev_b32_e32 v26, 16, v26
	v_lshrrev_b32_e32 v28, 16, v28
	v_and_or_b32 v26, v27, s27, v26
	v_and_or_b32 v27, v29, s27, v28
	global_store_dwordx2 v[48:49], v[26:27], off offset:512
	v_mul_f32_e32 v22, v22, v1
	v_mul_f32_e32 v23, v23, v1
	v_mul_f32_e32 v24, v24, v1
	v_mul_f32_e32 v25, v25, v1
	v_mul_f32_e32 v22, v68, v22
	v_mul_f32_e32 v23, v69, v23
	v_mul_f32_e32 v24, v70, v24
	v_mul_f32_e32 v25, v71, v25
	v_bfe_u32 v56, v22, 16, 1
	v_bfe_u32 v57, v23, 16, 1
	v_bfe_u32 v58, v24, 16, 1
	v_bfe_u32 v59, v25, 16, 1
	v_add3_u32 v22, v22, v56, s36
	v_add3_u32 v23, v23, v57, s36
	v_add3_u32 v24, v24, v58, s36
	v_add3_u32 v25, v25, v59, s36
	v_lshrrev_b32_e32 v22, 16, v22
	v_lshrrev_b32_e32 v24, 16, v24
	v_and_or_b32 v22, v23, s27, v22
	v_and_or_b32 v23, v25, s27, v24
	global_store_dwordx2 v[48:49], v[22:23], off offset:1024
	v_mul_f32_e32 v18, v18, v1
	v_mul_f32_e32 v19, v19, v1
	v_mul_f32_e32 v20, v20, v1
	v_mul_f32_e32 v21, v21, v1
	v_mul_f32_e32 v18, v72, v18
	v_mul_f32_e32 v19, v73, v19
	v_mul_f32_e32 v20, v74, v20
	v_mul_f32_e32 v21, v75, v21
	v_bfe_u32 v56, v18, 16, 1
	v_bfe_u32 v57, v19, 16, 1
	v_bfe_u32 v58, v20, 16, 1
	v_bfe_u32 v59, v21, 16, 1
	v_add3_u32 v18, v18, v56, s36
	v_add3_u32 v19, v19, v57, s36
	v_add3_u32 v20, v20, v58, s36
	v_add3_u32 v21, v21, v59, s36
	v_lshrrev_b32_e32 v18, 16, v18
	v_lshrrev_b32_e32 v20, 16, v20
	v_and_or_b32 v18, v19, s27, v18
	v_and_or_b32 v19, v21, s27, v20
	global_store_dwordx2 v[48:49], v[18:19], off offset:1536
	v_mul_f32_e32 v14, v14, v1
	v_mul_f32_e32 v15, v15, v1
	v_mul_f32_e32 v16, v16, v1
	v_mul_f32_e32 v17, v17, v1
	v_mul_f32_e32 v14, v76, v14
	v_mul_f32_e32 v15, v77, v15
	v_mul_f32_e32 v16, v78, v16
	v_mul_f32_e32 v17, v79, v17
	v_bfe_u32 v56, v14, 16, 1
	v_bfe_u32 v57, v15, 16, 1
	v_bfe_u32 v58, v16, 16, 1
	v_bfe_u32 v59, v17, 16, 1
	v_add3_u32 v14, v14, v56, s36
	v_add3_u32 v15, v15, v57, s36
	v_add3_u32 v16, v16, v58, s36
	v_add3_u32 v17, v17, v59, s36
	v_lshrrev_b32_e32 v14, 16, v14
	v_lshrrev_b32_e32 v16, 16, v16
	v_and_or_b32 v14, v15, s27, v14
	v_and_or_b32 v15, v17, s27, v16
	global_store_dwordx2 v[48:49], v[14:15], off offset:2048
	v_mul_f32_e32 v10, v10, v1
	v_mul_f32_e32 v11, v11, v1
	v_mul_f32_e32 v12, v12, v1
	v_mul_f32_e32 v13, v13, v1
	v_mul_f32_e32 v10, v80, v10
	v_mul_f32_e32 v11, v81, v11
	v_mul_f32_e32 v12, v82, v12
	v_mul_f32_e32 v13, v83, v13
	v_bfe_u32 v56, v10, 16, 1
	v_bfe_u32 v57, v11, 16, 1
	v_bfe_u32 v58, v12, 16, 1
	v_bfe_u32 v59, v13, 16, 1
	v_add3_u32 v10, v10, v56, s36
	v_add3_u32 v11, v11, v57, s36
	v_add3_u32 v12, v12, v58, s36
	v_add3_u32 v13, v13, v59, s36
	v_lshrrev_b32_e32 v10, 16, v10
	v_lshrrev_b32_e32 v12, 16, v12
	v_and_or_b32 v10, v11, s27, v10
	v_and_or_b32 v11, v13, s27, v12
	global_store_dwordx2 v[48:49], v[10:11], off offset:2560
	v_mul_f32_e32 v6, v6, v1
	v_mul_f32_e32 v7, v7, v1
	v_mul_f32_e32 v8, v8, v1
	v_mul_f32_e32 v9, v9, v1
	v_mul_f32_e32 v6, v84, v6
	v_mul_f32_e32 v7, v85, v7
	v_mul_f32_e32 v8, v86, v8
	v_mul_f32_e32 v9, v87, v9
	v_bfe_u32 v56, v6, 16, 1
	v_bfe_u32 v57, v7, 16, 1
	v_bfe_u32 v58, v8, 16, 1
	v_bfe_u32 v59, v9, 16, 1
	v_add3_u32 v6, v6, v56, s36
	v_add3_u32 v7, v7, v57, s36
	v_add3_u32 v8, v8, v58, s36
	v_add3_u32 v9, v9, v59, s36
	v_lshrrev_b32_e32 v6, 16, v6
	v_lshrrev_b32_e32 v8, 16, v8
	v_and_or_b32 v6, v7, s27, v6
	v_and_or_b32 v7, v9, s27, v8
	global_store_dwordx2 v[48:49], v[6:7], off offset:3072
	v_mul_f32_e32 v2, v2, v1
	v_mul_f32_e32 v3, v3, v1
	v_mul_f32_e32 v4, v4, v1
	v_mul_f32_e32 v5, v5, v1
	v_mul_f32_e32 v2, v88, v2
	v_mul_f32_e32 v3, v89, v3
	v_mul_f32_e32 v4, v90, v4
	v_mul_f32_e32 v5, v91, v5
	v_bfe_u32 v56, v2, 16, 1
	v_bfe_u32 v57, v3, 16, 1
	v_bfe_u32 v58, v4, 16, 1
	v_bfe_u32 v59, v5, 16, 1
	v_add3_u32 v2, v2, v56, s36
	v_add3_u32 v3, v3, v57, s36
	v_add3_u32 v4, v4, v58, s36
	v_add3_u32 v5, v5, v59, s36
	v_lshrrev_b32_e32 v2, 16, v2
	v_lshrrev_b32_e32 v4, 16, v4
	v_and_or_b32 v2, v3, s27, v2
	v_and_or_b32 v3, v5, s27, v4
	global_store_dwordx2 v[48:49], v[2:3], off offset:3584
	s_cbranch_scc0 .LBB0_780

; __device__ __forceinline__ float rms_row_load(const float* xrow, int lane, f32x4 (&v)[8]) {
;     const f32x4* xr = (const f32x4*)xrow + lane; float s = 0.f;
; #pragma unroll
;     for (int j = 0; j < 8; ++j) { v[j] = xr[64 * j]; s += (v[j].x * v[j].x + v[j].y * v[j].y) + (v[j].z * v[j].z + v[j].w * v[j].w); }
;     return 1.0f / sqrtf(wave_sum(s) * (1.0f / D) + EPS);
.LBB0_1354:
	v_lshl_add_u64 v[2:3], s[4:5], 0, v[46:47]
	v_add_co_u32_e32 v4, vcc, 0x36da1000, v2
	s_add_i32 s6, s6, s8
	s_nop 0
	v_addc_co_u32_e32 v5, vcc, 0, v3, vcc
	global_load_dwordx4 v[30:33], v[4:5], off nt
	global_load_dwordx4 v[26:29], v[4:5], off offset:1024 nt
	global_load_dwordx4 v[22:25], v[4:5], off offset:2048 nt
	global_load_dwordx4 v[18:21], v[4:5], off offset:3072 nt
	v_add_co_u32_e32 v2, vcc, s10, v2
	v_lshl_add_u64 v[46:47], v[46:47], 0, s[14:15]
	s_nop 0
	v_addc_co_u32_e32 v3, vcc, 0, v3, vcc
	global_load_dwordx4 v[14:17], v[2:3], off nt
	global_load_dwordx4 v[10:13], v[2:3], off offset:1024 nt
	global_load_dwordx4 v[6:9], v[2:3], off offset:2048 nt
	global_load_dwordx4 v[2:5], v[2:3], off offset:3072 nt
	s_cmpk_gt_i32 s6, 0x1fff
	v_lshl_add_u64 v[48:49], s[4:5], 0, v[44:45]
	v_add_co_u32_e32 v48, vcc, s11, v48
	s_nop 1
	v_addc_co_u32_e32 v49, vcc, 0, v49, vcc
	v_lshl_add_u64 v[44:45], v[44:45], 0, s[12:13]
	s_waitcnt vmcnt(7)
	v_mul_f32_e32 v1, v31, v31
	v_mul_f32_e32 v57, v33, v33
	v_fmac_f32_e32 v1, v30, v30
	v_fmac_f32_e32 v57, v32, v32
	v_add_f32_e32 v1, v1, v57
	s_waitcnt vmcnt(6)
	v_mul_f32_e32 v56, v27, v27
	v_mul_f32_e32 v57, v29, v29
	v_fmac_f32_e32 v56, v26, v26
	v_fmac_f32_e32 v57, v28, v28
	v_add_f32_e32 v56, v56, v57
	v_add_f32_e32 v1, v1, v56
	s_waitcnt vmcnt(5)
	v_mul_f32_e32 v56, v23, v23
	v_mul_f32_e32 v57, v25, v25
	v_fmac_f32_e32 v56, v22, v22
	v_fmac_f32_e32 v57, v24, v24
	v_add_f32_e32 v56, v56, v57
	v_add_f32_e32 v1, v1, v56
	s_waitcnt vmcnt(4)
	v_mul_f32_e32 v56, v19, v19
	v_mul_f32_e32 v57, v21, v21
	v_fmac_f32_e32 v56, v18, v18
	v_fmac_f32_e32 v57, v20, v20
	v_add_f32_e32 v56, v56, v57
	v_add_f32_e32 v1, v1, v56
	s_waitcnt vmcnt(3)
	v_mul_f32_e32 v56, v15, v15
	v_mul_f32_e32 v57, v17, v17
	v_fmac_f32_e32 v56, v14, v14
	v_fmac_f32_e32 v57, v16, v16
	v_add_f32_e32 v56, v56, v57
	v_add_f32_e32 v1, v1, v56
	s_waitcnt vmcnt(2)
	v_mul_f32_e32 v56, v11, v11
	v_mul_f32_e32 v57, v13, v13
	v_fmac_f32_e32 v56, v10, v10
	v_fmac_f32_e32 v57, v12, v12
	v_add_f32_e32 v56, v56, v57
	v_add_f32_e32 v1, v1, v56
	s_waitcnt vmcnt(1)
	v_mul_f32_e32 v56, v7, v7
	v_mul_f32_e32 v57, v9, v9
	v_fmac_f32_e32 v56, v6, v6
	v_fmac_f32_e32 v57, v8, v8
	v_add_f32_e32 v56, v56, v57
	v_add_f32_e32 v1, v1, v56
	s_waitcnt vmcnt(0)
	v_mul_f32_e32 v56, v3, v3
	v_mul_f32_e32 v57, v5, v5
	v_fmac_f32_e32 v56, v2, v2
	v_fmac_f32_e32 v57, v4, v4
	v_add_f32_e32 v56, v56, v57
	v_add_f32_e32 v1, v1, v56
	ds_bpermute_b32 v56, v50, v1
	s_waitcnt lgkmcnt(0)
	v_add_f32_e32 v1, v1, v56
	ds_bpermute_b32 v56, v51, v1
	s_waitcnt lgkmcnt(0)
	v_add_f32_e32 v1, v1, v56
	ds_bpermute_b32 v56, v52, v1
	s_waitcnt lgkmcnt(0)
	v_add_f32_e32 v1, v1, v56
	ds_bpermute_b32 v56, v53, v1
	s_waitcnt lgkmcnt(0)
	v_add_f32_e32 v1, v1, v56
	ds_bpermute_b32 v56, v54, v1
	s_waitcnt lgkmcnt(0)
	v_add_f32_e32 v1, v1, v56
	ds_bpermute_b32 v56, v55, v1
	s_waitcnt lgkmcnt(0)
; __device__ __forceinline__ unsigned pk2(float lo, float hi) { return f2bf(lo) | (f2bf(hi) << 16); }
; __device__ __forceinline__ void rms_row_to_bf16(const float* xrow, const float* gain, bf16* orow, int lane) {
;     f32x4 v[8]; const float rstd = rms_row_load(xrow, lane, v);
;     const f32x4* gr = (const f32x4*)gain + lane; unsigned long long* o8 = (unsigned long long*)orow + lane;
; #pragma unroll
;     for (int j = 0; j < 8; ++j) { const f32x4 g = gr[64 * j]; o8[64 * j] = (unsigned long long)pk2(v[j].x * rstd * g.x, v[j].y * rstd * g.y) | ((unsigned long long)pk2(v[j].z * rstd * g.z, v[j].w * rstd * g.w) << 32); }
	v_add_f32_e32 v1, v1, v56
	v_fmamk_f32 v1, v1, 0x3a000000, v226
	v_cmp_gt_f32_e32 vcc, s9, v1
	v_mul_f32_e32 v92, 0x4f800000, v1
	s_nop 0
	v_cndmask_b32_e32 v1, v1, v92, vcc
	v_sqrt_f32_e32 v92, v1
	s_nop 0
	v_add_u32_e32 v93, -1, v92
	v_fma_f32 v56, -v93, v92, v1
	v_cmp_ge_f32_e64 s[0:1], 0, v56
	v_add_u32_e32 v56, 1, v92
	s_nop 0
	v_cndmask_b32_e64 v93, v92, v93, s[0:1]
	v_fma_f32 v92, -v56, v92, v1
	v_cmp_lt_f32_e64 s[0:1], 0, v92
	s_nop 1
	v_cndmask_b32_e64 v92, v93, v56, s[0:1]
	v_mul_f32_e32 v93, 0x37800000, v92
	v_cndmask_b32_e32 v92, v92, v93, vcc
	v_cmp_class_f32_e32 vcc, v1, v225
	s_nop 1
	v_cndmask_b32_e32 v1, v92, v1, vcc
	v_div_scale_f32 v92, s[0:1], v1, v1, 1.0
	v_rcp_f32_e32 v93, v92
	s_nop 0
	v_fma_f32 v56, -v92, v93, 1.0
	v_fmac_f32_e32 v93, v56, v93
	v_div_scale_f32 v56, vcc, 1.0, v1, 1.0
	v_mul_f32_e32 v57, v56, v93
	v_fma_f32 v58, -v92, v57, v56
	v_fmac_f32_e32 v57, v58, v93
	v_fma_f32 v92, -v92, v57, v56
	v_div_fmas_f32 v92, v92, v93, v57
	v_div_fixup_f32 v1, v92, v1, 1.0
	v_mul_f32_e32 v30, v30, v1
	v_mul_f32_e32 v31, v31, v1
	v_mul_f32_e32 v32, v32, v1
	v_mul_f32_e32 v33, v33, v1
	v_mul_f32_e32 v30, v60, v30
	v_mul_f32_e32 v31, v61, v31
	v_mul_f32_e32 v32, v62, v32
	v_mul_f32_e32 v33, v63, v33
	v_bfe_u32 v56, v30, 16, 1
	v_bfe_u32 v57, v31, 16, 1
	v_bfe_u32 v58, v32, 16, 1
	v_bfe_u32 v59, v33, 16, 1
	v_add3_u32 v30, v30, v56, s36
	v_add3_u32 v31, v31, v57, s36
	v_add3_u32 v32, v32, v58, s36
	v_add3_u32 v33, v33, v59, s36
	v_lshrrev_b32_e32 v30, 16, v30
	v_lshrrev_b32_e32 v32, 16, v32
	v_and_or_b32 v30, v31, s27, v30
	v_and_or_b32 v31, v33, s27, v32
	global_store_dwordx2 v[48:49], v[30:31], off
	v_mul_f32_e32 v26, v26, v1
	v_mul_f32_e32 v27, v27, v1
	v_mul_f32_e32 v28, v28, v1
	v_mul_f32_e32 v29, v29, v1
	v_mul_f32_e32 v26, v64, v26
	v_mul_f32_e32 v27, v65, v27
	v_mul_f32_e32 v28, v66, v28
	v_mul_f32_e32 v29, v67, v29
	v_bfe_u32 v56, v26, 16, 1
	v_bfe_u32 v57, v27, 16, 1
	v_bfe_u32 v58, v28, 16, 1
	v_bfe_u32 v59, v29, 16, 1
	v_add3_u32 v26, v26, v56, s36
	v_add3_u32 v27, v27, v57, s36
	v_add3_u32 v28, v28, v58, s36
	v_add3_u32 v29, v29, v59, s36
	v_lshrrev_b32_e32 v26, 16, v26
	v_lshrrev_b32_e32 v28, 16, v28
	v_and_or_b32 v26, v27, s27, v26
	v_and_or_b32 v27, v29, s27, v28
	global_store_dwordx2 v[48:49], v[26:27], off offset:512
	v_mul_f32_e32 v22, v22, v1
	v_mul_f32_e32 v23, v23, v1
	v_mul_f32_e32 v24, v24, v1
	v_mul_f32_e32 v25, v25, v1
	v_mul_f32_e32 v22, v68, v22
	v_mul_f32_e32 v23, v69, v23
	v_mul_f32_e32 v24, v70, v24
	v_mul_f32_e32 v25, v71, v25
	v_bfe_u32 v56, v22, 16, 1
	v_bfe_u32 v57, v23, 16, 1
	v_bfe_u32 v58, v24, 16, 1
	v_bfe_u32 v59, v25, 16, 1
	v_add3_u32 v22, v22, v56, s36
	v_add3_u32 v23, v23, v57, s36
	v_add3_u32 v24, v24, v58, s36
	v_add3_u32 v25, v25, v59, s36
	v_lshrrev_b32_e32 v22, 16, v22
	v_lshrrev_b32_e32 v24, 16, v24
	v_and_or_b32 v22, v23, s27, v22
	v_and_or_b32 v23, v25, s27, v24
	global_store_dwordx2 v[48:49], v[22:23], off offset:1024
	v_mul_f32_e32 v18, v18, v1
	v_mul_f32_e32 v19, v19, v1
	v_mul_f32_e32 v20, v20, v1
	v_mul_f32_e32 v21, v21, v1
	v_mul_f32_e32 v18, v72, v18
	v_mul_f32_e32 v19, v73, v19
	v_mul_f32_e32 v20, v74, v20
	v_mul_f32_e32 v21, v75, v21
	v_bfe_u32 v56, v18, 16, 1
	v_bfe_u32 v57, v19, 16, 1
	v_bfe_u32 v58, v20, 16, 1
	v_bfe_u32 v59, v21, 16, 1
	v_add3_u32 v18, v18, v56, s36
	v_add3_u32 v19, v19, v57, s36
	v_add3_u32 v20, v20, v58, s36
	v_add3_u32 v21, v21, v59, s36
	v_lshrrev_b32_e32 v18, 16, v18
	v_lshrrev_b32_e32 v20, 16, v20
	v_and_or_b32 v18, v19, s27, v18
	v_and_or_b32 v19, v21, s27, v20
	global_store_dwordx2 v[48:49], v[18:19], off offset:1536
	v_mul_f32_e32 v14, v14, v1
	v_mul_f32_e32 v15, v15, v1
	v_mul_f32_e32 v16, v16, v1
	v_mul_f32_e32 v17, v17, v1
	v_mul_f32_e32 v14, v76, v14
	v_mul_f32_e32 v15, v77, v15
	v_mul_f32_e32 v16, v78, v16
	v_mul_f32_e32 v17, v79, v17
	v_bfe_u32 v56, v14, 16, 1
	v_bfe_u32 v57, v15, 16, 1
	v_bfe_u32 v58, v16, 16, 1
	v_bfe_u32 v59, v17, 16, 1
	v_add3_u32 v14, v14, v56, s36
	v_add3_u32 v15, v15, v57, s36
	v_add3_u32 v16, v16, v58, s36
	v_add3_u32 v17, v17, v59, s36
	v_lshrrev_b32_e32 v14, 16, v14
	v_lshrrev_b32_e32 v16, 16, v16
	v_and_or_b32 v14, v15, s27, v14
	v_and_or_b32 v15, v17, s27, v16
	global_store_dwordx2 v[48:49], v[14:15], off offset:2048
	v_mul_f32_e32 v10, v10, v1
	v_mul_f32_e32 v11, v11, v1
	v_mul_f32_e32 v12, v12, v1
	v_mul_f32_e32 v13, v13, v1
	v_mul_f32_e32 v10, v80, v10
	v_mul_f32_e32 v11, v81, v11
	v_mul_f32_e32 v12, v82, v12
	v_mul_f32_e32 v13, v83, v13
	v_bfe_u32 v56, v10, 16, 1
	v_bfe_u32 v57, v11, 16, 1
	v_bfe_u32 v58, v12, 16, 1
	v_bfe_u32 v59, v13, 16, 1
	v_add3_u32 v10, v10, v56, s36
	v_add3_u32 v11, v11, v57, s36
	v_add3_u32 v12, v12, v58, s36
	v_add3_u32 v13, v13, v59, s36
	v_lshrrev_b32_e32 v10, 16, v10
	v_lshrrev_b32_e32 v12, 16, v12
	v_and_or_b32 v10, v11, s27, v10
	v_and_or_b32 v11, v13, s27, v12
	global_store_dwordx2 v[48:49], v[10:11], off offset:2560
	v_mul_f32_e32 v6, v6, v1
	v_mul_f32_e32 v7, v7, v1
	v_mul_f32_e32 v8, v8, v1
	v_mul_f32_e32 v9, v9, v1
	v_mul_f32_e32 v6, v84, v6
	v_mul_f32_e32 v7, v85, v7
	v_mul_f32_e32 v8, v86, v8
	v_mul_f32_e32 v9, v87, v9
	v_bfe_u32 v56, v6, 16, 1
	v_bfe_u32 v57, v7, 16, 1
	v_bfe_u32 v58, v8, 16, 1
	v_bfe_u32 v59, v9, 16, 1
	v_add3_u32 v6, v6, v56, s36
	v_add3_u32 v7, v7, v57, s36
	v_add3_u32 v8, v8, v58, s36
	v_add3_u32 v9, v9, v59, s36
	v_lshrrev_b32_e32 v6, 16, v6
	v_lshrrev_b32_e32 v8, 16, v8
	v_and_or_b32 v6, v7, s27, v6
	v_and_or_b32 v7, v9, s27, v8
	global_store_dwordx2 v[48:49], v[6:7], off offset:3072
	v_mul_f32_e32 v2, v2, v1
	v_mul_f32_e32 v3, v3, v1
	v_mul_f32_e32 v4, v4, v1
	v_mul_f32_e32 v5, v5, v1
	v_mul_f32_e32 v2, v88, v2
	v_mul_f32_e32 v3, v89, v3
	v_mul_f32_e32 v4, v90, v4
	v_mul_f32_e32 v5, v91, v5
	v_bfe_u32 v56, v2, 16, 1
	v_bfe_u32 v57, v3, 16, 1
	v_bfe_u32 v58, v4, 16, 1
	v_bfe_u32 v59, v5, 16, 1
	v_add3_u32 v2, v2, v56, s36
	v_add3_u32 v3, v3, v57, s36
	v_add3_u32 v4, v4, v58, s36
	v_add3_u32 v5, v5, v59, s36
	v_lshrrev_b32_e32 v2, 16, v2
	v_lshrrev_b32_e32 v4, 16, v4
	v_and_or_b32 v2, v3, s27, v2
	v_and_or_b32 v3, v5, s27, v4
	global_store_dwordx2 v[48:49], v[2:3], off offset:3584
	s_cbranch_scc0 .LBB0_1354
